# v5 + GEMM main loops: per-MFMA-block s_setprio 1/0 flips deleted (timing-only)
# speedup vs baseline: 1.0025x; 1.0021x over previous
; #define PG8_STAGE(bufoff, gbase, voff) do { _Pragma("unroll") for (int _i = 0; _i < 2; ++_i) \
;         __builtin_amdgcn_global_load_lds((const unsigned*)((const char*)(gbase) + (voff)[_i]), (PG8_LAS unsigned*)(lds + (bufoff) + ldsw + _i * 8192), 16, 0, 0); } while (0)
; #define PG8_LDA(dst, b, h) do { _Pragma("unroll") for (int m = 0; m < 4; ++m) _Pragma("unroll") for (int k = 0; k < 2; ++k) dst[m][k] = *(const PG8_LAS bf16x8*)(lds + PG8_SA(b, h) + aoff + m * 2048 + k * 1024); } while (0)
; #define PG8_LDB(dst, b, h) do { _Pragma("unroll") for (int n = 0; n < 2; ++n) _Pragma("unroll") for (int k = 0; k < 2; ++k) dst[n][k] = *(const PG8_LAS bf16x8*)(lds + PG8_SB(b, h) + boff + n * 2048 + k * 1024); } while (0)
; #define PG8_MMA(ai, bj, At, Bt) do { __builtin_amdgcn_s_setprio(1); _Pragma("unroll") for (int m = 0; m < 4; ++m) _Pragma("unroll") for (int n = 0; n < 2; ++n) _Pragma("unroll") for (int k = 0; k < 2; ++k) \
;         acc[ai][bj][m][n] = mma16<I8>(Bt[n][k], At[m][k], acc[ai][bj][m][n]); __builtin_amdgcn_s_setprio(0); } while (0)
; #define PG8_WAIT_V(n) asm volatile("s_waitcnt vmcnt(" #n ")" ::: "memory")
; #define PG8_WAIT_L(n) asm volatile("s_waitcnt lgkmcnt(" #n ")" ::: "memory")
; #define PG8_BAR __builtin_amdgcn_s_barrier()
; #define PG8_SCHED __builtin_amdgcn_sched_barrier(0)
; template <class Epi, class Sched, bool ALIGN_EPI = false, bool SP2 = false, bool I8 = false>
; __device__ __forceinline__ void gemm_phase(PG8_LAS unsigned char* lds, const Gemm g, const Sched& S, const Epi& E) {
;     ...
;             PG8_LDB(B0, 0, 0); PG8_LDB(B1, 0, 1); PG8_SCHED; PG8_LDA(At, 0, 0); PG8_STAGE(PG8_SA(1, 1), a1 + hstep, voffA);
;             PG8_WAIT_V(8); PG8_WAIT_L(0); PG8_BAR; PG8_MMA(0, 0, At, B0); PG8_MMA(0, 1, At, B1); PG8_BAR; PG8_SCHED;
;             PG8_LDA(At, 0, 1); PG8_STAGE(PG8_SB(0, 0), b2, voffB); PG8_STAGE(PG8_SB(0, 1), b2 + hstep, voffB); PG8_STAGE(PG8_SA(0, 0), a2, voffA);
;             PG8_WAIT_V(8); PG8_WAIT_L(0); PG8_BAR; PG8_MMA(1, 0, At, B0); PG8_MMA(1, 1, At, B1); PG8_BAR; PG8_SCHED;
.LBB0_276:
	ds_read_b128 v[22:25], v203
	ds_read_b128 v[30:33], v203 offset:1024
	ds_read_b128 v[34:37], v203 offset:2048
	ds_read_b128 v[38:41], v203 offset:3072
	ds_read_b128 v[168:171], v204
	ds_read_b128 v[172:175], v204 offset:1024
	ds_read_b128 v[176:179], v204 offset:2048
	ds_read_b128 v[180:183], v204 offset:3072
	s_add_u32 s47, s42, 0xfffc0080
	s_addc_u32 s48, s43, -1
	s_cmp_eq_u32 s46, 12
	s_cselect_b32 s69, s5, s48
	s_cselect_b32 s68, s33, s47
	s_cselect_b32 s63, s35, s45
	s_cselect_b32 s62, s37, s44
	v_lshl_add_u64 v[226:227], s[42:43], 0, v[160:161]
	s_add_i32 m0, s3, 0xc000
	ds_read_b128 v[184:187], v205
	ds_read_b128 v[188:191], v205 offset:1024
	ds_read_b128 v[192:195], v205 offset:2048
	ds_read_b128 v[206:209], v205 offset:3072
	ds_read_b128 v[210:213], v205 offset:4096
	ds_read_b128 v[214:217], v205 offset:5120
	ds_read_b128 v[218:221], v205 offset:6144
	ds_read_b128 v[222:225], v205 offset:7168
	global_load_lds_dwordx4 v[226:227], off
	v_lshl_add_u64 v[226:227], s[42:43], 0, v[162:163]
	s_add_i32 m0, s3, 0xe000
	s_nop 0
	global_load_lds_dwordx4 v[226:227], off
	s_waitcnt vmcnt(8)
	s_waitcnt lgkmcnt(0)
	s_barrier
	s_waitcnt lgkmcnt(0)
	v_mfma_i32_16x16x64_i8 v[142:145], v[22:25], v[184:187], v[142:145]
	v_mfma_i32_16x16x64_i8 v[138:141], v[34:37], v[184:187], v[138:141]
	v_mfma_i32_16x16x64_i8 v[126:129], v[22:25], v[192:195], v[126:129]
	v_mfma_i32_16x16x64_i8 v[122:125], v[34:37], v[192:195], v[122:125]
	v_mfma_i32_16x16x64_i8 v[110:113], v[22:25], v[210:213], v[110:113]
	v_mfma_i32_16x16x64_i8 v[106:109], v[34:37], v[210:213], v[106:109]
	v_mfma_i32_16x16x64_i8 v[94:97], v[22:25], v[218:221], v[94:97]
	v_mfma_i32_16x16x64_i8 v[90:93], v[34:37], v[218:221], v[90:93]
	v_mfma_i32_16x16x64_i8 v[142:145], v[30:33], v[188:191], v[142:145]
	v_mfma_i32_16x16x64_i8 v[138:141], v[38:41], v[188:191], v[138:141]
	v_mfma_i32_16x16x64_i8 v[126:129], v[30:33], v[206:209], v[126:129]
	v_mfma_i32_16x16x64_i8 v[122:125], v[38:41], v[206:209], v[122:125]
	v_mfma_i32_16x16x64_i8 v[110:113], v[30:33], v[214:217], v[110:113]
	v_mfma_i32_16x16x64_i8 v[106:109], v[38:41], v[214:217], v[106:109]
	v_mfma_i32_16x16x64_i8 v[94:97], v[30:33], v[222:225], v[94:97]
	v_mfma_i32_16x16x64_i8 v[90:93], v[38:41], v[222:225], v[90:93]
	v_mfma_i32_16x16x64_i8 v[134:137], v[168:171], v[184:187], v[134:137]
	v_mfma_i32_16x16x64_i8 v[130:133], v[176:179], v[184:187], v[130:133]
	v_mfma_i32_16x16x64_i8 v[118:121], v[168:171], v[192:195], v[118:121]
	v_mfma_i32_16x16x64_i8 v[114:117], v[176:179], v[192:195], v[114:117]
	v_mfma_i32_16x16x64_i8 v[102:105], v[168:171], v[210:213], v[102:105]
	v_mfma_i32_16x16x64_i8 v[98:101], v[176:179], v[210:213], v[98:101]
	v_mfma_i32_16x16x64_i8 v[86:89], v[168:171], v[218:221], v[86:89]
	v_mfma_i32_16x16x64_i8 v[82:85], v[176:179], v[218:221], v[82:85]
	v_mfma_i32_16x16x64_i8 v[134:137], v[172:175], v[188:191], v[134:137]
	v_mfma_i32_16x16x64_i8 v[130:133], v[180:183], v[188:191], v[130:133]
	v_mfma_i32_16x16x64_i8 v[118:121], v[172:175], v[206:209], v[118:121]
	v_mfma_i32_16x16x64_i8 v[114:117], v[180:183], v[206:209], v[114:117]
	v_mfma_i32_16x16x64_i8 v[102:105], v[172:175], v[214:217], v[102:105]
	v_mfma_i32_16x16x64_i8 v[98:101], v[180:183], v[214:217], v[98:101]
	v_mfma_i32_16x16x64_i8 v[86:89], v[172:175], v[222:225], v[86:89]
	v_mfma_i32_16x16x64_i8 v[82:85], v[180:183], v[222:225], v[82:85]
	s_barrier
	s_add_i32 s47, s84, s19
	v_lshl_add_u64 v[226:227], s[62:63], 0, v[154:155]
	s_mov_b32 m0, s47
	ds_read_b128 v[184:187], v205 offset:16384
	ds_read_b128 v[188:191], v205 offset:17408
	ds_read_b128 v[192:195], v205 offset:18432
	ds_read_b128 v[206:209], v205 offset:19456
	ds_read_b128 v[210:213], v205 offset:20480
	ds_read_b128 v[214:217], v205 offset:21504
	ds_read_b128 v[218:221], v205 offset:22528
	ds_read_b128 v[222:225], v205 offset:23552
	global_load_lds_dwordx4 v[226:227], off
	s_add_i32 m0, s47, 0x2000
	s_add_u32 s48, s62, 0x40000
	v_lshl_add_u64 v[228:229], s[62:63], 0, v[158:159]
	s_addc_u32 s49, s63, 0
	s_add_i32 s47, s85, s19
	global_load_lds_dwordx4 v[228:229], off
	v_lshl_add_u64 v[230:231], s[48:49], 0, v[154:155]
	s_mov_b32 m0, s47
	v_lshl_add_u64 v[232:233], s[68:69], 0, v[156:157]
	global_load_lds_dwordx4 v[230:231], off
	v_lshl_add_u64 v[230:231], s[48:49], 0, v[158:159]
	s_add_i32 m0, s47, 0x2000
	s_nop 0
	global_load_lds_dwordx4 v[230:231], off
	v_lshl_add_u64 v[230:231], s[68:69], 0, v[152:153]
	s_mov_b32 m0, s3
	s_nop 0
	global_load_lds_dwordx4 v[230:231], off
	s_mov_b32 m0, s21
	s_nop 0
	global_load_lds_dwordx4 v[232:233], off
	s_waitcnt vmcnt(8)
	s_waitcnt lgkmcnt(0)
	s_barrier
; #define PG8_STAGE(bufoff, gbase, voff) do { _Pragma("unroll") for (int _i = 0; _i < 2; ++_i) \
;         __builtin_amdgcn_global_load_lds((const unsigned*)((const char*)(gbase) + (voff)[_i]), (PG8_LAS unsigned*)(lds + (bufoff) + ldsw + _i * 8192), 16, 0, 0); } while (0)
; #define PG8_LDA(dst, b, h) do { _Pragma("unroll") for (int m = 0; m < 4; ++m) _Pragma("unroll") for (int k = 0; k < 2; ++k) dst[m][k] = *(const PG8_LAS bf16x8*)(lds + PG8_SA(b, h) + aoff + m * 2048 + k * 1024); } while (0)
; #define PG8_LDB(dst, b, h) do { _Pragma("unroll") for (int n = 0; n < 2; ++n) _Pragma("unroll") for (int k = 0; k < 2; ++k) dst[n][k] = *(const PG8_LAS bf16x8*)(lds + PG8_SB(b, h) + boff + n * 2048 + k * 1024); } while (0)
; #define PG8_MMA(ai, bj, At, Bt) do { __builtin_amdgcn_s_setprio(1); _Pragma("unroll") for (int m = 0; m < 4; ++m) _Pragma("unroll") for (int n = 0; n < 2; ++n) _Pragma("unroll") for (int k = 0; k < 2; ++k) \
;         acc[ai][bj][m][n] = mma16<I8>(Bt[n][k], At[m][k], acc[ai][bj][m][n]); __builtin_amdgcn_s_setprio(0); } while (0)
; #define PG8_WAIT_V(n) asm volatile("s_waitcnt vmcnt(" #n ")" ::: "memory")
; #define PG8_WAIT_L(n) asm volatile("s_waitcnt lgkmcnt(" #n ")" ::: "memory")
; #define PG8_BAR __builtin_amdgcn_s_barrier()
; #define PG8_SCHED __builtin_amdgcn_sched_barrier(0)
; template <class Epi, class Sched, bool ALIGN_EPI = false, bool SP2 = false, bool I8 = false>
; __device__ __forceinline__ void gemm_phase(PG8_LAS unsigned char* lds, const Gemm g, const Sched& S, const Epi& E) {
;     ...
;             PG8_WAIT_V(8); PG8_WAIT_L(0); PG8_BAR; PG8_MMA(1, 0, At, B0); PG8_MMA(1, 1, At, B1); PG8_BAR; PG8_SCHED;
;             PG8_LDB(B0, 1, 0); PG8_LDB(B1, 1, 1); PG8_SCHED; PG8_LDA(At, 1, 0); PG8_STAGE(PG8_SA(0, 1), a2 + hstep, voffA);
;             PG8_WAIT_V(8); PG8_WAIT_L(0); PG8_BAR; PG8_MMA(0, 0, At, B0); PG8_MMA(0, 1, At, B1); PG8_BAR; PG8_SCHED;
	s_waitcnt lgkmcnt(0)
	v_mfma_i32_16x16x64_i8 v[78:81], v[22:25], v[184:187], v[78:81]
	v_mfma_i32_16x16x64_i8 v[74:77], v[34:37], v[184:187], v[74:77]
	v_mfma_i32_16x16x64_i8 v[62:65], v[22:25], v[192:195], v[62:65]
	v_mfma_i32_16x16x64_i8 v[58:61], v[34:37], v[192:195], v[58:61]
	v_mfma_i32_16x16x64_i8 v[46:49], v[22:25], v[210:213], v[46:49]
	v_mfma_i32_16x16x64_i8 v[42:45], v[34:37], v[210:213], v[42:45]
	v_mfma_i32_16x16x64_i8 v[14:17], v[22:25], v[218:221], v[14:17]
	v_mfma_i32_16x16x64_i8 v[10:13], v[34:37], v[218:221], v[10:13]
	v_mfma_i32_16x16x64_i8 v[78:81], v[30:33], v[188:191], v[78:81]
	v_mfma_i32_16x16x64_i8 v[74:77], v[38:41], v[188:191], v[74:77]
	v_mfma_i32_16x16x64_i8 v[62:65], v[30:33], v[206:209], v[62:65]
	v_mfma_i32_16x16x64_i8 v[58:61], v[38:41], v[206:209], v[58:61]
	v_mfma_i32_16x16x64_i8 v[46:49], v[30:33], v[214:217], v[46:49]
	v_mfma_i32_16x16x64_i8 v[42:45], v[38:41], v[214:217], v[42:45]
	v_mfma_i32_16x16x64_i8 v[14:17], v[30:33], v[222:225], v[14:17]
	v_mfma_i32_16x16x64_i8 v[10:13], v[38:41], v[222:225], v[10:13]
	v_mfma_i32_16x16x64_i8 v[26:29], v[168:171], v[210:213], v[26:29]
	v_mfma_i32_16x16x64_i8 v[18:21], v[176:179], v[210:213], v[18:21]
	v_mfma_i32_16x16x64_i8 v[6:9], v[168:171], v[218:221], v[6:9]
	v_mfma_i32_16x16x64_i8 v[2:5], v[176:179], v[218:221], v[2:5]
	v_mfma_i32_16x16x64_i8 v[22:25], v[168:171], v[184:187], v[70:73]
	v_mfma_i32_16x16x64_i8 v[30:33], v[176:179], v[184:187], v[66:69]
	v_mfma_i32_16x16x64_i8 v[34:37], v[168:171], v[192:195], v[54:57]
	v_mfma_i32_16x16x64_i8 v[38:41], v[176:179], v[192:195], v[50:53]
	v_mfma_i32_16x16x64_i8 v[26:29], v[172:175], v[214:217], v[26:29]
	v_mfma_i32_16x16x64_i8 v[18:21], v[180:183], v[214:217], v[18:21]
	v_mfma_i32_16x16x64_i8 v[6:9], v[172:175], v[222:225], v[6:9]
	v_mfma_i32_16x16x64_i8 v[2:5], v[180:183], v[222:225], v[2:5]
	v_mfma_i32_16x16x64_i8 v[22:25], v[172:175], v[188:191], v[22:25]
	v_mfma_i32_16x16x64_i8 v[30:33], v[180:183], v[188:191], v[30:33]
	v_mfma_i32_16x16x64_i8 v[34:37], v[172:175], v[206:209], v[34:37]
	v_mfma_i32_16x16x64_i8 v[38:41], v[180:183], v[206:209], v[38:41]
	s_barrier
	s_add_i32 s47, 0, 0x18000
	s_add_i32 s50, 0, 0x1c000
	v_add_u32_e32 v70, s47, v201
	v_add_u32_e32 v180, s50, v201
	ds_read_b128 v[50:53], v70
	ds_read_b128 v[54:57], v70 offset:1024
	ds_read_b128 v[66:69], v70 offset:2048
	ds_read_b128 v[70:73], v70 offset:3072
	ds_read_b128 v[168:171], v180
	ds_read_b128 v[172:175], v180 offset:1024
	ds_read_b128 v[176:179], v180 offset:2048
	ds_read_b128 v[180:183], v180 offset:3072
	s_add_u32 s48, s68, 0x40000
	s_addc_u32 s49, s69, 0
	s_mov_b32 m0, s23
	v_lshl_add_u64 v[234:235], s[48:49], 0, v[152:153]
	ds_read_b128 v[184:187], v205 offset:32768
	ds_read_b128 v[188:191], v205 offset:33792
	ds_read_b128 v[192:195], v205 offset:34816
	ds_read_b128 v[206:209], v205 offset:35840
	ds_read_b128 v[210:213], v205 offset:36864
	ds_read_b128 v[214:217], v205 offset:37888
	ds_read_b128 v[218:221], v205 offset:38912
	ds_read_b128 v[222:225], v205 offset:39936
	global_load_lds_dwordx4 v[234:235], off
	v_lshl_add_u64 v[234:235], s[48:49], 0, v[156:157]
	s_mov_b32 m0, s25
	s_nop 0
	global_load_lds_dwordx4 v[234:235], off
	s_waitcnt vmcnt(8)
	s_waitcnt lgkmcnt(0)
	s_barrier
	s_waitcnt lgkmcnt(0)
	v_mfma_i32_16x16x64_i8 v[142:145], v[50:53], v[184:187], v[142:145]
	v_mfma_i32_16x16x64_i8 v[138:141], v[66:69], v[184:187], v[138:141]
	v_mfma_i32_16x16x64_i8 v[126:129], v[50:53], v[192:195], v[126:129]
	v_mfma_i32_16x16x64_i8 v[122:125], v[66:69], v[192:195], v[122:125]
	v_mfma_i32_16x16x64_i8 v[110:113], v[50:53], v[210:213], v[110:113]
	v_mfma_i32_16x16x64_i8 v[106:109], v[66:69], v[210:213], v[106:109]
	v_mfma_i32_16x16x64_i8 v[94:97], v[50:53], v[218:221], v[94:97]
	v_mfma_i32_16x16x64_i8 v[90:93], v[66:69], v[218:221], v[90:93]
	v_mfma_i32_16x16x64_i8 v[142:145], v[54:57], v[188:191], v[142:145]
	v_mfma_i32_16x16x64_i8 v[138:141], v[70:73], v[188:191], v[138:141]
	v_mfma_i32_16x16x64_i8 v[126:129], v[54:57], v[206:209], v[126:129]
	v_mfma_i32_16x16x64_i8 v[122:125], v[70:73], v[206:209], v[122:125]
	v_mfma_i32_16x16x64_i8 v[110:113], v[54:57], v[214:217], v[110:113]
	v_mfma_i32_16x16x64_i8 v[106:109], v[70:73], v[214:217], v[106:109]
	v_mfma_i32_16x16x64_i8 v[94:97], v[54:57], v[222:225], v[94:97]
	v_mfma_i32_16x16x64_i8 v[90:93], v[70:73], v[222:225], v[90:93]
	v_mfma_i32_16x16x64_i8 v[134:137], v[168:171], v[184:187], v[134:137]
	v_mfma_i32_16x16x64_i8 v[130:133], v[176:179], v[184:187], v[130:133]
	v_mfma_i32_16x16x64_i8 v[118:121], v[168:171], v[192:195], v[118:121]
	v_mfma_i32_16x16x64_i8 v[114:117], v[176:179], v[192:195], v[114:117]
	v_mfma_i32_16x16x64_i8 v[102:105], v[168:171], v[210:213], v[102:105]
	v_mfma_i32_16x16x64_i8 v[98:101], v[176:179], v[210:213], v[98:101]
	v_mfma_i32_16x16x64_i8 v[86:89], v[168:171], v[218:221], v[86:89]
	v_mfma_i32_16x16x64_i8 v[82:85], v[176:179], v[218:221], v[82:85]
	v_mfma_i32_16x16x64_i8 v[134:137], v[172:175], v[188:191], v[134:137]
	v_mfma_i32_16x16x64_i8 v[130:133], v[180:183], v[188:191], v[130:133]
	v_mfma_i32_16x16x64_i8 v[118:121], v[172:175], v[206:209], v[118:121]
	v_mfma_i32_16x16x64_i8 v[114:117], v[180:183], v[206:209], v[114:117]
	v_mfma_i32_16x16x64_i8 v[102:105], v[172:175], v[214:217], v[102:105]
	v_mfma_i32_16x16x64_i8 v[98:101], v[180:183], v[214:217], v[98:101]
	v_mfma_i32_16x16x64_i8 v[86:89], v[172:175], v[222:225], v[86:89]
	v_mfma_i32_16x16x64_i8 v[82:85], v[180:183], v[222:225], v[82:85]
	s_barrier
; #define PG8_STAGE(bufoff, gbase, voff) do { _Pragma("unroll") for (int _i = 0; _i < 2; ++_i) \
;         __builtin_amdgcn_global_load_lds((const unsigned*)((const char*)(gbase) + (voff)[_i]), (PG8_LAS unsigned*)(lds + (bufoff) + ldsw + _i * 8192), 16, 0, 0); } while (0)
; #define PG8_LDA(dst, b, h) do { _Pragma("unroll") for (int m = 0; m < 4; ++m) _Pragma("unroll") for (int k = 0; k < 2; ++k) dst[m][k] = *(const PG8_LAS bf16x8*)(lds + PG8_SA(b, h) + aoff + m * 2048 + k * 1024); } while (0)
; #define PG8_MMA(ai, bj, At, Bt) do { __builtin_amdgcn_s_setprio(1); _Pragma("unroll") for (int m = 0; m < 4; ++m) _Pragma("unroll") for (int n = 0; n < 2; ++n) _Pragma("unroll") for (int k = 0; k < 2; ++k) \
;         acc[ai][bj][m][n] = mma16<I8>(Bt[n][k], At[m][k], acc[ai][bj][m][n]); __builtin_amdgcn_s_setprio(0); } while (0)
; #define PG8_WAIT_V(n) asm volatile("s_waitcnt vmcnt(" #n ")" ::: "memory")
; #define PG8_WAIT_L(n) asm volatile("s_waitcnt lgkmcnt(" #n ")" ::: "memory")
; #define PG8_BAR __builtin_amdgcn_s_barrier()
; #define PG8_SCHED __builtin_amdgcn_sched_barrier(0)
; template <class Epi, class Sched, bool ALIGN_EPI = false, bool SP2 = false, bool I8 = false>
; __device__ __forceinline__ void gemm_phase(PG8_LAS unsigned char* lds, const Gemm g, const Sched& S, const Epi& E) {
;     ...
;         for (int t = 0; t < nt; t += 2) {
;     ...
;             PG8_LDA(At, 1, 1); PG8_STAGE(PG8_SB(1, 0), b3, voffB); PG8_STAGE(PG8_SB(1, 1), b3 + hstep, voffB); PG8_STAGE(PG8_SA(1, 0), a3, voffA);
;             PG8_WAIT_V(8); PG8_WAIT_L(0); PG8_BAR; PG8_MMA(1, 0, At, B0); PG8_MMA(1, 1, At, B1); PG8_BAR; PG8_SCHED;
	s_add_i32 s47, s47, s19
	v_lshl_add_u64 v[226:227], v[226:227], 0, s[14:15]
	s_mov_b32 m0, s47
	ds_read_b128 v[184:187], v205 offset:49152
	ds_read_b128 v[188:191], v205 offset:50176
	ds_read_b128 v[192:195], v205 offset:51200
	ds_read_b128 v[206:209], v205 offset:52224
	ds_read_b128 v[210:213], v205 offset:53248
	ds_read_b128 v[214:217], v205 offset:54272
	ds_read_b128 v[218:221], v205 offset:55296
	ds_read_b128 v[222:225], v205 offset:56320
	global_load_lds_dwordx4 v[226:227], off
	s_add_i32 m0, s47, 0x2000
	s_add_u32 s48, s62, 0x40080
	v_lshl_add_u64 v[226:227], v[228:229], 0, s[14:15]
	s_addc_u32 s49, s63, 0
	s_add_i32 s47, s50, s19
	global_load_lds_dwordx4 v[226:227], off
	v_lshl_add_u64 v[226:227], s[48:49], 0, v[154:155]
	s_mov_b32 m0, s47
	s_nop 0
	global_load_lds_dwordx4 v[226:227], off
	v_lshl_add_u64 v[226:227], s[48:49], 0, v[158:159]
	s_add_i32 m0, s47, 0x2000
	s_nop 0
	global_load_lds_dwordx4 v[226:227], off
	v_lshl_add_u64 v[226:227], v[230:231], 0, s[14:15]
	s_mov_b32 m0, s29
	s_nop 0
	global_load_lds_dwordx4 v[226:227], off
	v_lshl_add_u64 v[226:227], v[232:233], 0, s[14:15]
	s_mov_b32 m0, s31
	s_nop 0
	global_load_lds_dwordx4 v[226:227], off
	s_waitcnt vmcnt(8)
	s_waitcnt lgkmcnt(0)
	s_barrier
	s_waitcnt lgkmcnt(0)
	v_mfma_i32_16x16x64_i8 v[78:81], v[50:53], v[184:187], v[78:81]
	v_mfma_i32_16x16x64_i8 v[74:77], v[66:69], v[184:187], v[74:77]
	v_mfma_i32_16x16x64_i8 v[62:65], v[50:53], v[192:195], v[62:65]
	v_mfma_i32_16x16x64_i8 v[58:61], v[66:69], v[192:195], v[58:61]
	v_mfma_i32_16x16x64_i8 v[46:49], v[50:53], v[210:213], v[46:49]
	v_mfma_i32_16x16x64_i8 v[42:45], v[66:69], v[210:213], v[42:45]
	v_mfma_i32_16x16x64_i8 v[14:17], v[50:53], v[218:221], v[14:17]
	v_mfma_i32_16x16x64_i8 v[10:13], v[66:69], v[218:221], v[10:13]
	v_mfma_i32_16x16x64_i8 v[78:81], v[54:57], v[188:191], v[78:81]
	v_mfma_i32_16x16x64_i8 v[74:77], v[70:73], v[188:191], v[74:77]
	v_mfma_i32_16x16x64_i8 v[62:65], v[54:57], v[206:209], v[62:65]
	v_mfma_i32_16x16x64_i8 v[58:61], v[70:73], v[206:209], v[58:61]
	v_mfma_i32_16x16x64_i8 v[46:49], v[54:57], v[214:217], v[46:49]
	v_mfma_i32_16x16x64_i8 v[42:45], v[70:73], v[214:217], v[42:45]
	v_mfma_i32_16x16x64_i8 v[14:17], v[54:57], v[222:225], v[14:17]
	v_mfma_i32_16x16x64_i8 v[10:13], v[70:73], v[222:225], v[10:13]
	v_mfma_i32_16x16x64_i8 v[22:25], v[168:171], v[184:187], v[22:25]
	v_mfma_i32_16x16x64_i8 v[70:73], v[172:175], v[188:191], v[22:25]
	v_mfma_i32_16x16x64_i8 v[22:25], v[176:179], v[184:187], v[30:33]
	v_mfma_i32_16x16x64_i8 v[66:69], v[180:183], v[188:191], v[22:25]
	v_mfma_i32_16x16x64_i8 v[22:25], v[168:171], v[192:195], v[34:37]
	v_mfma_i32_16x16x64_i8 v[54:57], v[172:175], v[206:209], v[22:25]
	v_mfma_i32_16x16x64_i8 v[22:25], v[176:179], v[192:195], v[38:41]
	v_mfma_i32_16x16x64_i8 v[50:53], v[180:183], v[206:209], v[22:25]
	v_mfma_i32_16x16x64_i8 v[22:25], v[168:171], v[210:213], v[26:29]
	v_mfma_i32_16x16x64_i8 v[18:21], v[176:179], v[210:213], v[18:21]
	v_mfma_i32_16x16x64_i8 v[6:9], v[168:171], v[218:221], v[6:9]
	v_mfma_i32_16x16x64_i8 v[2:5], v[176:179], v[218:221], v[2:5]
	v_mfma_i32_16x16x64_i8 v[26:29], v[172:175], v[214:217], v[22:25]
	v_mfma_i32_16x16x64_i8 v[18:21], v[180:183], v[214:217], v[18:21]
	v_mfma_i32_16x16x64_i8 v[6:9], v[172:175], v[222:225], v[6:9]
	v_mfma_i32_16x16x64_i8 v[2:5], v[180:183], v[222:225], v[2:5]
	s_barrier
	s_add_i32 s46, s46, 2
	s_add_u32 s42, s42, 0x100
	s_addc_u32 s43, s43, 0
	s_add_u32 s44, s44, 0x100
	s_addc_u32 s45, s45, 0
	s_cmp_gt_u32 s46, 13
	s_cbranch_scc0 .LBB0_276
	s_and_b64 vcc, exec, s[16:17]
	s_cbranch_vccz .LBB0_279
	s_barrier

; #define PG8_STAGE(bufoff, gbase, voff) do { _Pragma("unroll") for (int _i = 0; _i < 2; ++_i) \
;         __builtin_amdgcn_global_load_lds((const unsigned*)((const char*)(gbase) + (voff)[_i]), (PG8_LAS unsigned*)(lds + (bufoff) + ldsw + _i * 8192), 16, 0, 0); } while (0)
; #define PG8_LDA(dst, b, h) do { _Pragma("unroll") for (int m = 0; m < 4; ++m) _Pragma("unroll") for (int k = 0; k < 2; ++k) dst[m][k] = *(const PG8_LAS bf16x8*)(lds + PG8_SA(b, h) + aoff + m * 2048 + k * 1024); } while (0)
; #define PG8_LDB(dst, b, h) do { _Pragma("unroll") for (int n = 0; n < 2; ++n) _Pragma("unroll") for (int k = 0; k < 2; ++k) dst[n][k] = *(const PG8_LAS bf16x8*)(lds + PG8_SB(b, h) + boff + n * 2048 + k * 1024); } while (0)
; #define PG8_MMA(ai, bj, At, Bt) do { __builtin_amdgcn_s_setprio(1); _Pragma("unroll") for (int m = 0; m < 4; ++m) _Pragma("unroll") for (int n = 0; n < 2; ++n) _Pragma("unroll") for (int k = 0; k < 2; ++k) \
;         acc[ai][bj][m][n] = mma16<I8>(Bt[n][k], At[m][k], acc[ai][bj][m][n]); __builtin_amdgcn_s_setprio(0); } while (0)
; #define PG8_WAIT_V(n) asm volatile("s_waitcnt vmcnt(" #n ")" ::: "memory")
; #define PG8_WAIT_L(n) asm volatile("s_waitcnt lgkmcnt(" #n ")" ::: "memory")
; #define PG8_BAR __builtin_amdgcn_s_barrier()
; #define PG8_SCHED __builtin_amdgcn_sched_barrier(0)
; template <class Epi, class Sched, bool ALIGN_EPI = false, bool SP2 = false, bool I8 = false>
; __device__ __forceinline__ void gemm_phase(PG8_LAS unsigned char* lds, const Gemm g, const Sched& S, const Epi& E) {
;     ...
;             PG8_LDB(B0, 0, 0); PG8_LDB(B1, 0, 1); PG8_SCHED; PG8_LDA(At, 0, 0); PG8_STAGE(PG8_SA(1, 1), a1 + hstep, voffA);
;             PG8_WAIT_V(8); PG8_WAIT_L(0); PG8_BAR; PG8_MMA(0, 0, At, B0); PG8_MMA(0, 1, At, B1); PG8_BAR; PG8_SCHED;
;             PG8_LDA(At, 0, 1); PG8_STAGE(PG8_SB(0, 0), b2, voffB); PG8_STAGE(PG8_SB(0, 1), b2 + hstep, voffB); PG8_STAGE(PG8_SA(0, 0), a2, voffA);
;             PG8_WAIT_V(8); PG8_WAIT_L(0); PG8_BAR; PG8_MMA(1, 0, At, B0); PG8_MMA(1, 1, At, B1); PG8_BAR; PG8_SCHED;
.LBB0_334:
	ds_read_b128 v[22:25], v1
	ds_read_b128 v[26:29], v1 offset:1024
	ds_read_b128 v[34:37], v1 offset:2048
	ds_read_b128 v[38:41], v1 offset:3072
	ds_read_b128 v[168:171], v147
	ds_read_b128 v[172:175], v147 offset:1024
	ds_read_b128 v[176:179], v147 offset:2048
	ds_read_b128 v[180:183], v147 offset:3072
	s_add_u32 s42, s40, 0xfffc0080
	s_addc_u32 s43, s41, -1
	s_cmp_eq_u32 s46, 12
	s_cselect_b32 s63, s5, s43
	s_cselect_b32 s62, s33, s42
	s_cselect_b32 s43, s31, s45
	s_cselect_b32 s42, s35, s44
	v_lshl_add_u64 v[198:199], s[40:41], 0, v[160:161]
	s_add_i32 m0, s3, 0xc000
	ds_read_b128 v[184:187], v149
	ds_read_b128 v[188:191], v149 offset:1024
	ds_read_b128 v[192:195], v149 offset:2048
	ds_read_b128 v[202:205], v149 offset:3072
	ds_read_b128 v[206:209], v149 offset:4096
	ds_read_b128 v[210:213], v149 offset:5120
	ds_read_b128 v[214:217], v149 offset:6144
	ds_read_b128 v[218:221], v149 offset:7168
	global_load_lds_dwordx4 v[198:199], off
	v_lshl_add_u64 v[198:199], s[40:41], 0, v[162:163]
	s_add_i32 m0, s3, 0xe000
	s_nop 0
	global_load_lds_dwordx4 v[198:199], off
	s_waitcnt vmcnt(8)
	s_waitcnt lgkmcnt(0)
	s_barrier
	s_waitcnt lgkmcnt(0)
	v_mfma_i32_16x16x64_i8 v[142:145], v[22:25], v[184:187], v[142:145]
	v_mfma_i32_16x16x64_i8 v[138:141], v[34:37], v[184:187], v[138:141]
	v_mfma_i32_16x16x64_i8 v[126:129], v[22:25], v[192:195], v[126:129]
	v_mfma_i32_16x16x64_i8 v[122:125], v[34:37], v[192:195], v[122:125]
	v_mfma_i32_16x16x64_i8 v[110:113], v[22:25], v[206:209], v[110:113]
	v_mfma_i32_16x16x64_i8 v[106:109], v[34:37], v[206:209], v[106:109]
	v_mfma_i32_16x16x64_i8 v[94:97], v[22:25], v[214:217], v[94:97]
	v_mfma_i32_16x16x64_i8 v[90:93], v[34:37], v[214:217], v[90:93]
	v_mfma_i32_16x16x64_i8 v[142:145], v[26:29], v[188:191], v[142:145]
	v_mfma_i32_16x16x64_i8 v[138:141], v[38:41], v[188:191], v[138:141]
	v_mfma_i32_16x16x64_i8 v[126:129], v[26:29], v[202:205], v[126:129]
	v_mfma_i32_16x16x64_i8 v[122:125], v[38:41], v[202:205], v[122:125]
	v_mfma_i32_16x16x64_i8 v[110:113], v[26:29], v[210:213], v[110:113]
	v_mfma_i32_16x16x64_i8 v[106:109], v[38:41], v[210:213], v[106:109]
	v_mfma_i32_16x16x64_i8 v[94:97], v[26:29], v[218:221], v[94:97]
	v_mfma_i32_16x16x64_i8 v[90:93], v[38:41], v[218:221], v[90:93]
	v_mfma_i32_16x16x64_i8 v[134:137], v[168:171], v[184:187], v[134:137]
	v_mfma_i32_16x16x64_i8 v[130:133], v[176:179], v[184:187], v[130:133]
	v_mfma_i32_16x16x64_i8 v[118:121], v[168:171], v[192:195], v[118:121]
	v_mfma_i32_16x16x64_i8 v[114:117], v[176:179], v[192:195], v[114:117]
	v_mfma_i32_16x16x64_i8 v[102:105], v[168:171], v[206:209], v[102:105]
	v_mfma_i32_16x16x64_i8 v[98:101], v[176:179], v[206:209], v[98:101]
	v_mfma_i32_16x16x64_i8 v[86:89], v[168:171], v[214:217], v[86:89]
	v_mfma_i32_16x16x64_i8 v[82:85], v[176:179], v[214:217], v[82:85]
	v_mfma_i32_16x16x64_i8 v[134:137], v[172:175], v[188:191], v[134:137]
	v_mfma_i32_16x16x64_i8 v[130:133], v[180:183], v[188:191], v[130:133]
	v_mfma_i32_16x16x64_i8 v[118:121], v[172:175], v[202:205], v[118:121]
	v_mfma_i32_16x16x64_i8 v[114:117], v[180:183], v[202:205], v[114:117]
	v_mfma_i32_16x16x64_i8 v[102:105], v[172:175], v[210:213], v[102:105]
	v_mfma_i32_16x16x64_i8 v[98:101], v[180:183], v[210:213], v[98:101]
	v_mfma_i32_16x16x64_i8 v[86:89], v[172:175], v[218:221], v[86:89]
	v_mfma_i32_16x16x64_i8 v[82:85], v[180:183], v[218:221], v[82:85]
	s_barrier
	s_add_i32 s47, s84, s21
	v_lshl_add_u64 v[198:199], s[42:43], 0, v[154:155]
	s_mov_b32 m0, s47
	ds_read_b128 v[184:187], v149 offset:16384
	ds_read_b128 v[188:191], v149 offset:17408
	ds_read_b128 v[192:195], v149 offset:18432
	ds_read_b128 v[202:205], v149 offset:19456
	ds_read_b128 v[206:209], v149 offset:20480
	ds_read_b128 v[210:213], v149 offset:21504
	ds_read_b128 v[214:217], v149 offset:22528
	ds_read_b128 v[218:221], v149 offset:23552
	global_load_lds_dwordx4 v[198:199], off
	s_add_i32 m0, s47, 0x2000
	s_add_u32 s48, s42, 0x40000
	v_lshl_add_u64 v[222:223], s[42:43], 0, v[158:159]
	s_addc_u32 s49, s43, 0
	s_add_i32 s47, s85, s21
	global_load_lds_dwordx4 v[222:223], off
	v_lshl_add_u64 v[224:225], s[48:49], 0, v[154:155]
	s_mov_b32 m0, s47
	v_lshl_add_u64 v[226:227], s[62:63], 0, v[156:157]
	global_load_lds_dwordx4 v[224:225], off
	v_lshl_add_u64 v[224:225], s[48:49], 0, v[158:159]
	s_add_i32 m0, s47, 0x2000
	s_nop 0
	global_load_lds_dwordx4 v[224:225], off
	v_lshl_add_u64 v[224:225], s[62:63], 0, v[152:153]
	s_mov_b32 m0, s3
	s_nop 0
	global_load_lds_dwordx4 v[224:225], off
	s_mov_b32 m0, s23
	s_nop 0
	global_load_lds_dwordx4 v[226:227], off
	s_waitcnt vmcnt(8)
	s_waitcnt lgkmcnt(0)
	s_barrier
; #define PG8_STAGE(bufoff, gbase, voff) do { _Pragma("unroll") for (int _i = 0; _i < 2; ++_i) \
;         __builtin_amdgcn_global_load_lds((const unsigned*)((const char*)(gbase) + (voff)[_i]), (PG8_LAS unsigned*)(lds + (bufoff) + ldsw + _i * 8192), 16, 0, 0); } while (0)
; #define PG8_LDA(dst, b, h) do { _Pragma("unroll") for (int m = 0; m < 4; ++m) _Pragma("unroll") for (int k = 0; k < 2; ++k) dst[m][k] = *(const PG8_LAS bf16x8*)(lds + PG8_SA(b, h) + aoff + m * 2048 + k * 1024); } while (0)
; #define PG8_LDB(dst, b, h) do { _Pragma("unroll") for (int n = 0; n < 2; ++n) _Pragma("unroll") for (int k = 0; k < 2; ++k) dst[n][k] = *(const PG8_LAS bf16x8*)(lds + PG8_SB(b, h) + boff + n * 2048 + k * 1024); } while (0)
; #define PG8_MMA(ai, bj, At, Bt) do { __builtin_amdgcn_s_setprio(1); _Pragma("unroll") for (int m = 0; m < 4; ++m) _Pragma("unroll") for (int n = 0; n < 2; ++n) _Pragma("unroll") for (int k = 0; k < 2; ++k) \
;         acc[ai][bj][m][n] = mma16<I8>(Bt[n][k], At[m][k], acc[ai][bj][m][n]); __builtin_amdgcn_s_setprio(0); } while (0)
; #define PG8_WAIT_V(n) asm volatile("s_waitcnt vmcnt(" #n ")" ::: "memory")
; #define PG8_WAIT_L(n) asm volatile("s_waitcnt lgkmcnt(" #n ")" ::: "memory")
; #define PG8_BAR __builtin_amdgcn_s_barrier()
; #define PG8_SCHED __builtin_amdgcn_sched_barrier(0)
; template <class Epi, class Sched, bool ALIGN_EPI = false, bool SP2 = false, bool I8 = false>
; __device__ __forceinline__ void gemm_phase(PG8_LAS unsigned char* lds, const Gemm g, const Sched& S, const Epi& E) {
;     ...
;             PG8_WAIT_V(8); PG8_WAIT_L(0); PG8_BAR; PG8_MMA(1, 0, At, B0); PG8_MMA(1, 1, At, B1); PG8_BAR; PG8_SCHED;
;             PG8_LDB(B0, 1, 0); PG8_LDB(B1, 1, 1); PG8_SCHED; PG8_LDA(At, 1, 0); PG8_STAGE(PG8_SA(0, 1), a2 + hstep, voffA);
;             PG8_WAIT_V(8); PG8_WAIT_L(0); PG8_BAR; PG8_MMA(0, 0, At, B0); PG8_MMA(0, 1, At, B1); PG8_BAR; PG8_SCHED;
	s_waitcnt lgkmcnt(0)
	v_mfma_i32_16x16x64_i8 v[78:81], v[22:25], v[184:187], v[78:81]
	v_mfma_i32_16x16x64_i8 v[74:77], v[34:37], v[184:187], v[74:77]
	v_mfma_i32_16x16x64_i8 v[62:65], v[22:25], v[192:195], v[62:65]
	v_mfma_i32_16x16x64_i8 v[58:61], v[34:37], v[192:195], v[58:61]
	v_mfma_i32_16x16x64_i8 v[46:49], v[22:25], v[206:209], v[46:49]
	v_mfma_i32_16x16x64_i8 v[42:45], v[34:37], v[206:209], v[42:45]
	v_mfma_i32_16x16x64_i8 v[14:17], v[22:25], v[214:217], v[14:17]
	v_mfma_i32_16x16x64_i8 v[10:13], v[34:37], v[214:217], v[10:13]
	v_mfma_i32_16x16x64_i8 v[78:81], v[26:29], v[188:191], v[78:81]
	v_mfma_i32_16x16x64_i8 v[74:77], v[38:41], v[188:191], v[74:77]
	v_mfma_i32_16x16x64_i8 v[62:65], v[26:29], v[202:205], v[62:65]
	v_mfma_i32_16x16x64_i8 v[58:61], v[38:41], v[202:205], v[58:61]
	v_mfma_i32_16x16x64_i8 v[46:49], v[26:29], v[210:213], v[46:49]
	v_mfma_i32_16x16x64_i8 v[42:45], v[38:41], v[210:213], v[42:45]
	v_mfma_i32_16x16x64_i8 v[14:17], v[26:29], v[218:221], v[14:17]
	v_mfma_i32_16x16x64_i8 v[10:13], v[38:41], v[218:221], v[10:13]
	v_mfma_i32_16x16x64_i8 v[30:33], v[168:171], v[206:209], v[30:33]
	v_mfma_i32_16x16x64_i8 v[18:21], v[176:179], v[206:209], v[18:21]
	v_mfma_i32_16x16x64_i8 v[6:9], v[168:171], v[214:217], v[6:9]
	v_mfma_i32_16x16x64_i8 v[2:5], v[176:179], v[214:217], v[2:5]
	v_mfma_i32_16x16x64_i8 v[22:25], v[168:171], v[184:187], v[70:73]
	v_mfma_i32_16x16x64_i8 v[26:29], v[176:179], v[184:187], v[66:69]
	v_mfma_i32_16x16x64_i8 v[34:37], v[168:171], v[192:195], v[54:57]
	v_mfma_i32_16x16x64_i8 v[38:41], v[176:179], v[192:195], v[50:53]
	v_mfma_i32_16x16x64_i8 v[30:33], v[172:175], v[210:213], v[30:33]
	v_mfma_i32_16x16x64_i8 v[18:21], v[180:183], v[210:213], v[18:21]
	v_mfma_i32_16x16x64_i8 v[6:9], v[172:175], v[218:221], v[6:9]
	v_mfma_i32_16x16x64_i8 v[2:5], v[180:183], v[218:221], v[2:5]
	v_mfma_i32_16x16x64_i8 v[22:25], v[172:175], v[188:191], v[22:25]
	v_mfma_i32_16x16x64_i8 v[26:29], v[180:183], v[188:191], v[26:29]
	v_mfma_i32_16x16x64_i8 v[34:37], v[172:175], v[202:205], v[34:37]
	v_mfma_i32_16x16x64_i8 v[38:41], v[180:183], v[202:205], v[38:41]
	s_barrier
	s_add_i32 s47, 0, 0x18000
	s_add_i32 s50, 0, 0x1c000
	v_add_u32_e32 v70, s47, v197
	v_add_u32_e32 v151, s50, v197
	ds_read_b128 v[50:53], v70
	ds_read_b128 v[54:57], v70 offset:1024
	ds_read_b128 v[66:69], v70 offset:2048
	ds_read_b128 v[70:73], v70 offset:3072
	ds_read_b128 v[168:171], v151
	ds_read_b128 v[172:175], v151 offset:1024
	ds_read_b128 v[176:179], v151 offset:2048
	ds_read_b128 v[180:183], v151 offset:3072
	s_add_u32 s48, s62, 0x40000
	s_addc_u32 s49, s63, 0
	s_mov_b32 m0, s25
	v_lshl_add_u64 v[228:229], s[48:49], 0, v[152:153]
	ds_read_b128 v[184:187], v149 offset:32768
	ds_read_b128 v[188:191], v149 offset:33792
	ds_read_b128 v[192:195], v149 offset:34816
	ds_read_b128 v[202:205], v149 offset:35840
	ds_read_b128 v[206:209], v149 offset:36864
	ds_read_b128 v[210:213], v149 offset:37888
	ds_read_b128 v[214:217], v149 offset:38912
	ds_read_b128 v[218:221], v149 offset:39936
	global_load_lds_dwordx4 v[228:229], off
	v_lshl_add_u64 v[228:229], s[48:49], 0, v[156:157]
	s_mov_b32 m0, s27
	s_nop 0
	global_load_lds_dwordx4 v[228:229], off
	s_waitcnt vmcnt(8)
	s_waitcnt lgkmcnt(0)
	s_barrier
	s_waitcnt lgkmcnt(0)
	v_mfma_i32_16x16x64_i8 v[142:145], v[50:53], v[184:187], v[142:145]
	v_mfma_i32_16x16x64_i8 v[138:141], v[66:69], v[184:187], v[138:141]
	v_mfma_i32_16x16x64_i8 v[126:129], v[50:53], v[192:195], v[126:129]
	v_mfma_i32_16x16x64_i8 v[122:125], v[66:69], v[192:195], v[122:125]
	v_mfma_i32_16x16x64_i8 v[110:113], v[50:53], v[206:209], v[110:113]
	v_mfma_i32_16x16x64_i8 v[106:109], v[66:69], v[206:209], v[106:109]
	v_mfma_i32_16x16x64_i8 v[94:97], v[50:53], v[214:217], v[94:97]
	v_mfma_i32_16x16x64_i8 v[90:93], v[66:69], v[214:217], v[90:93]
	v_mfma_i32_16x16x64_i8 v[142:145], v[54:57], v[188:191], v[142:145]
	v_mfma_i32_16x16x64_i8 v[138:141], v[70:73], v[188:191], v[138:141]
	v_mfma_i32_16x16x64_i8 v[126:129], v[54:57], v[202:205], v[126:129]
	v_mfma_i32_16x16x64_i8 v[122:125], v[70:73], v[202:205], v[122:125]
	v_mfma_i32_16x16x64_i8 v[110:113], v[54:57], v[210:213], v[110:113]
	v_mfma_i32_16x16x64_i8 v[106:109], v[70:73], v[210:213], v[106:109]
	v_mfma_i32_16x16x64_i8 v[94:97], v[54:57], v[218:221], v[94:97]
	v_mfma_i32_16x16x64_i8 v[90:93], v[70:73], v[218:221], v[90:93]
	v_mfma_i32_16x16x64_i8 v[134:137], v[168:171], v[184:187], v[134:137]
	v_mfma_i32_16x16x64_i8 v[130:133], v[176:179], v[184:187], v[130:133]
	v_mfma_i32_16x16x64_i8 v[118:121], v[168:171], v[192:195], v[118:121]
	v_mfma_i32_16x16x64_i8 v[114:117], v[176:179], v[192:195], v[114:117]
	v_mfma_i32_16x16x64_i8 v[102:105], v[168:171], v[206:209], v[102:105]
	v_mfma_i32_16x16x64_i8 v[98:101], v[176:179], v[206:209], v[98:101]
	v_mfma_i32_16x16x64_i8 v[86:89], v[168:171], v[214:217], v[86:89]
	v_mfma_i32_16x16x64_i8 v[82:85], v[176:179], v[214:217], v[82:85]
	v_mfma_i32_16x16x64_i8 v[134:137], v[172:175], v[188:191], v[134:137]
	v_mfma_i32_16x16x64_i8 v[130:133], v[180:183], v[188:191], v[130:133]
	v_mfma_i32_16x16x64_i8 v[118:121], v[172:175], v[202:205], v[118:121]
	v_mfma_i32_16x16x64_i8 v[114:117], v[180:183], v[202:205], v[114:117]
	v_mfma_i32_16x16x64_i8 v[102:105], v[172:175], v[210:213], v[102:105]
	v_mfma_i32_16x16x64_i8 v[98:101], v[180:183], v[210:213], v[98:101]
	v_mfma_i32_16x16x64_i8 v[86:89], v[172:175], v[218:221], v[86:89]
	v_mfma_i32_16x16x64_i8 v[82:85], v[180:183], v[218:221], v[82:85]
	s_barrier
; #define PG8_STAGE(bufoff, gbase, voff) do { _Pragma("unroll") for (int _i = 0; _i < 2; ++_i) \
;         __builtin_amdgcn_global_load_lds((const unsigned*)((const char*)(gbase) + (voff)[_i]), (PG8_LAS unsigned*)(lds + (bufoff) + ldsw + _i * 8192), 16, 0, 0); } while (0)
; #define PG8_LDA(dst, b, h) do { _Pragma("unroll") for (int m = 0; m < 4; ++m) _Pragma("unroll") for (int k = 0; k < 2; ++k) dst[m][k] = *(const PG8_LAS bf16x8*)(lds + PG8_SA(b, h) + aoff + m * 2048 + k * 1024); } while (0)
; #define PG8_WAIT_V(n) asm volatile("s_waitcnt vmcnt(" #n ")" ::: "memory")
; #define PG8_WAIT_L(n) asm volatile("s_waitcnt lgkmcnt(" #n ")" ::: "memory")
; #define PG8_BAR __builtin_amdgcn_s_barrier()
; template <class Epi, class Sched, bool ALIGN_EPI = false, bool SP2 = false, bool I8 = false>
; __device__ __forceinline__ void gemm_phase(PG8_LAS unsigned char* lds, const Gemm g, const Sched& S, const Epi& E) {
;     ...
;         for (int t = 0; t < nt; t += 2) {
;             const bool last = (t == nt - 2);
;             const char* a1 = cA + (size_t)(t + 1) * kstep;
;             const char* a2 = last ? nA : cA + (size_t)(t + 2) * kstep; const char* b2 = last ? nB : cB + (size_t)(t + 2) * kstep;
;             const char* a3 = a2 + kstep; const char* b3 = b2 + kstep;
;             if (last && has_next) S.a_ready(nxt);
;             if constexpr (SP2) {
;             PG8_LDB(B0, 0, 0); PG8_LDB(B1, 0, 1); PG8_SCHED; PG8_LDA(At, 0, 0); PG8_STAGE(PG8_SA(1, 1), a1 + hstep, voffA);
;             PG8_WAIT_V(8); PG8_WAIT_L(0); PG8_BAR; PG8_MMA(0, 0, At, B0); PG8_MMA(0, 1, At, B1); PG8_BAR; PG8_SCHED;
;             PG8_LDA(At, 0, 1); PG8_STAGE(PG8_SB(0, 0), b2, voffB); PG8_STAGE(PG8_SB(0, 1), b2 + hstep, voffB); PG8_STAGE(PG8_SA(0, 0), a2, voffA);
;             PG8_WAIT_V(8); PG8_WAIT_L(0); PG8_BAR; PG8_MMA(1, 0, At, B0); PG8_MMA(1, 1, At, B1); PG8_BAR; PG8_SCHED;
;             PG8_LDB(B0, 1, 0); PG8_LDB(B1, 1, 1); PG8_SCHED; PG8_LDA(At, 1, 0); PG8_STAGE(PG8_SA(0, 1), a2 + hstep, voffA);
;             PG8_WAIT_V(8); PG8_WAIT_L(0); PG8_BAR; PG8_MMA(0, 0, At, B0); PG8_MMA(0, 1, At, B1); PG8_BAR; PG8_SCHED;
;             PG8_LDA(At, 1, 1); PG8_STAGE(PG8_SB(1, 0), b3, voffB); PG8_STAGE(PG8_SB(1, 1), b3 + hstep, voffB); PG8_STAGE(PG8_SA(1, 0), a3, voffA);
;             PG8_WAIT_V(8); PG8_WAIT_L(0); PG8_BAR; PG8_MMA(1, 0, At, B0); PG8_MMA(1, 1, At, B1); PG8_BAR; PG8_SCHED;
	s_add_i32 s47, s47, s21
	v_lshl_add_u64 v[198:199], v[198:199], 0, s[12:13]
	s_mov_b32 m0, s47
	ds_read_b128 v[184:187], v149 offset:49152
	ds_read_b128 v[188:191], v149 offset:50176
	ds_read_b128 v[192:195], v149 offset:51200
	ds_read_b128 v[202:205], v149 offset:52224
	ds_read_b128 v[206:209], v149 offset:53248
	ds_read_b128 v[210:213], v149 offset:54272
	ds_read_b128 v[214:217], v149 offset:55296
	ds_read_b128 v[218:221], v149 offset:56320
	global_load_lds_dwordx4 v[198:199], off
	s_add_i32 m0, s47, 0x2000
	s_add_u32 s42, s42, 0x40080
	v_lshl_add_u64 v[198:199], v[222:223], 0, s[12:13]
	s_addc_u32 s43, s43, 0
	s_add_i32 s47, s50, s21
	global_load_lds_dwordx4 v[198:199], off
	v_lshl_add_u64 v[198:199], s[42:43], 0, v[154:155]
	s_mov_b32 m0, s47
	s_nop 0
	global_load_lds_dwordx4 v[198:199], off
	v_lshl_add_u64 v[198:199], s[42:43], 0, v[158:159]
	s_add_i32 m0, s47, 0x2000
	s_nop 0
	global_load_lds_dwordx4 v[198:199], off
	v_lshl_add_u64 v[198:199], v[224:225], 0, s[12:13]
	s_mov_b32 m0, s68
	s_nop 0
	global_load_lds_dwordx4 v[198:199], off
	v_lshl_add_u64 v[198:199], v[226:227], 0, s[12:13]
	s_mov_b32 m0, s69
	s_nop 0
	global_load_lds_dwordx4 v[198:199], off
	s_waitcnt vmcnt(8)
	s_waitcnt lgkmcnt(0)
	s_barrier
	s_waitcnt lgkmcnt(0)
	v_mfma_i32_16x16x64_i8 v[78:81], v[50:53], v[184:187], v[78:81]
	v_mfma_i32_16x16x64_i8 v[74:77], v[66:69], v[184:187], v[74:77]
	v_mfma_i32_16x16x64_i8 v[62:65], v[50:53], v[192:195], v[62:65]
	v_mfma_i32_16x16x64_i8 v[58:61], v[66:69], v[192:195], v[58:61]
	v_mfma_i32_16x16x64_i8 v[46:49], v[50:53], v[206:209], v[46:49]
	v_mfma_i32_16x16x64_i8 v[42:45], v[66:69], v[206:209], v[42:45]
	v_mfma_i32_16x16x64_i8 v[14:17], v[50:53], v[214:217], v[14:17]
	v_mfma_i32_16x16x64_i8 v[10:13], v[66:69], v[214:217], v[10:13]
	v_mfma_i32_16x16x64_i8 v[78:81], v[54:57], v[188:191], v[78:81]
	v_mfma_i32_16x16x64_i8 v[74:77], v[70:73], v[188:191], v[74:77]
	v_mfma_i32_16x16x64_i8 v[62:65], v[54:57], v[202:205], v[62:65]
	v_mfma_i32_16x16x64_i8 v[58:61], v[70:73], v[202:205], v[58:61]
	v_mfma_i32_16x16x64_i8 v[46:49], v[54:57], v[210:213], v[46:49]
	v_mfma_i32_16x16x64_i8 v[42:45], v[70:73], v[210:213], v[42:45]
	v_mfma_i32_16x16x64_i8 v[14:17], v[54:57], v[218:221], v[14:17]
	v_mfma_i32_16x16x64_i8 v[10:13], v[70:73], v[218:221], v[10:13]
	v_mfma_i32_16x16x64_i8 v[22:25], v[168:171], v[184:187], v[22:25]
	v_mfma_i32_16x16x64_i8 v[70:73], v[172:175], v[188:191], v[22:25]
	v_mfma_i32_16x16x64_i8 v[22:25], v[176:179], v[184:187], v[26:29]
	v_mfma_i32_16x16x64_i8 v[66:69], v[180:183], v[188:191], v[22:25]
	v_mfma_i32_16x16x64_i8 v[22:25], v[168:171], v[192:195], v[34:37]
	v_mfma_i32_16x16x64_i8 v[54:57], v[172:175], v[202:205], v[22:25]
	v_mfma_i32_16x16x64_i8 v[22:25], v[176:179], v[192:195], v[38:41]
	v_mfma_i32_16x16x64_i8 v[50:53], v[180:183], v[202:205], v[22:25]
	v_mfma_i32_16x16x64_i8 v[22:25], v[168:171], v[206:209], v[30:33]
	v_mfma_i32_16x16x64_i8 v[18:21], v[176:179], v[206:209], v[18:21]
	v_mfma_i32_16x16x64_i8 v[6:9], v[168:171], v[214:217], v[6:9]
	v_mfma_i32_16x16x64_i8 v[2:5], v[176:179], v[214:217], v[2:5]
	v_mfma_i32_16x16x64_i8 v[30:33], v[172:175], v[210:213], v[22:25]
	v_mfma_i32_16x16x64_i8 v[18:21], v[180:183], v[210:213], v[18:21]
	v_mfma_i32_16x16x64_i8 v[6:9], v[172:175], v[218:221], v[6:9]
	v_mfma_i32_16x16x64_i8 v[2:5], v[180:183], v[218:221], v[2:5]
	s_barrier
	s_add_i32 s46, s46, 2
	s_add_u32 s40, s40, 0x100
	s_addc_u32 s41, s41, 0
	s_add_u32 s44, s44, 0x100
	s_addc_u32 s45, s45, 0
	s_cmp_gt_u32 s46, 13
	s_cbranch_scc0 .LBB0_334
	s_and_b64 vcc, exec, s[14:15]
	s_cbranch_vccz .LBB0_337
	s_barrier

; #define PG8_STAGE(bufoff, gbase, voff) do { _Pragma("unroll") for (int _i = 0; _i < 2; ++_i) \
;         __builtin_amdgcn_global_load_lds((const unsigned*)((const char*)(gbase) + (voff)[_i]), (PG8_LAS unsigned*)(lds + (bufoff) + ldsw + _i * 8192), 16, 0, 0); } while (0)
; #define PG8_LDA(dst, b, h) do { _Pragma("unroll") for (int m = 0; m < 4; ++m) _Pragma("unroll") for (int k = 0; k < 2; ++k) dst[m][k] = *(const PG8_LAS bf16x8*)(lds + PG8_SA(b, h) + aoff + m * 2048 + k * 1024); } while (0)
; #define PG8_LDB(dst, b, h) do { _Pragma("unroll") for (int n = 0; n < 2; ++n) _Pragma("unroll") for (int k = 0; k < 2; ++k) dst[n][k] = *(const PG8_LAS bf16x8*)(lds + PG8_SB(b, h) + boff + n * 2048 + k * 1024); } while (0)
; #define PG8_MMA(ai, bj, At, Bt) do { __builtin_amdgcn_s_setprio(1); _Pragma("unroll") for (int m = 0; m < 4; ++m) _Pragma("unroll") for (int n = 0; n < 2; ++n) _Pragma("unroll") for (int k = 0; k < 2; ++k) \
;         acc[ai][bj][m][n] = mma16<I8>(Bt[n][k], At[m][k], acc[ai][bj][m][n]); __builtin_amdgcn_s_setprio(0); } while (0)
; #define PG8_WAIT_V(n) asm volatile("s_waitcnt vmcnt(" #n ")" ::: "memory")
; #define PG8_WAIT_L(n) asm volatile("s_waitcnt lgkmcnt(" #n ")" ::: "memory")
; #define PG8_BAR __builtin_amdgcn_s_barrier()
; #define PG8_SCHED __builtin_amdgcn_sched_barrier(0)
; template <class Epi, class Sched, bool ALIGN_EPI = false, bool SP2 = false, bool I8 = false>
; __device__ __forceinline__ void gemm_phase(PG8_LAS unsigned char* lds, const Gemm g, const Sched& S, const Epi& E) {
;     ...
;             PG8_LDB(B0, 0, 0); PG8_LDB(B1, 0, 1); PG8_SCHED; PG8_LDA(At, 0, 0); PG8_STAGE(PG8_SA(1, 1), a1 + hstep, voffA);
;             PG8_WAIT_V(8); PG8_WAIT_L(0); PG8_BAR; PG8_MMA(0, 0, At, B0); PG8_MMA(0, 1, At, B1); PG8_BAR; PG8_SCHED;
;             PG8_LDA(At, 0, 1); PG8_STAGE(PG8_SB(0, 0), b2, voffB); PG8_STAGE(PG8_SB(0, 1), b2 + hstep, voffB); PG8_STAGE(PG8_SA(0, 0), a2, voffA);
;             PG8_WAIT_V(8); PG8_WAIT_L(0); PG8_BAR; PG8_MMA(1, 0, At, B0); PG8_MMA(1, 1, At, B1); PG8_BAR; PG8_SCHED;
.LBB0_974:
	ds_read_b128 v[130:133], v163
	ds_read_b128 v[134:137], v163 offset:1024
	ds_read_b128 v[164:167], v163 offset:2048
	ds_read_b128 v[168:171], v163 offset:3072
	ds_read_b128 v[172:175], v181
	ds_read_b128 v[176:179], v181 offset:1024
	ds_read_b128 v[184:187], v181 offset:2048
	ds_read_b128 v[188:191], v181 offset:3072
	s_add_u32 s42, s40, 0xfffc0080
	s_addc_u32 s43, s41, -1
	s_cmp_eq_u32 s63, 12
	s_cselect_b32 s45, s31, s43
	s_cselect_b32 s44, s57, s42
	s_cselect_b32 s43, s29, s62
	s_cselect_b32 s42, s58, s59
	v_lshl_add_u64 v[160:161], s[40:41], 0, v[152:153]
	s_add_i32 m0, s39, 0xc000
	ds_read_b128 v[192:195], v183
	ds_read_b128 v[202:205], v183 offset:1024
	ds_read_b128 v[206:209], v183 offset:2048
	ds_read_b128 v[210:213], v183 offset:3072
	ds_read_b128 v[214:217], v183 offset:4096
	ds_read_b128 v[218:221], v183 offset:5120
	ds_read_b128 v[222:225], v183 offset:6144
	ds_read_b128 v[226:229], v183 offset:7168
	global_load_lds_dwordx4 v[160:161], off
	v_lshl_add_u64 v[160:161], s[40:41], 0, v[154:155]
	s_add_i32 m0, s39, 0xe000
	s_nop 0
	global_load_lds_dwordx4 v[160:161], off
	s_waitcnt vmcnt(8)
	s_waitcnt lgkmcnt(0)
	s_barrier
	s_waitcnt lgkmcnt(0)
	v_mfma_i32_16x16x64_i8 v[126:129], v[130:133], v[192:195], v[126:129]
	v_mfma_i32_16x16x64_i8 v[122:125], v[164:167], v[192:195], v[122:125]
	v_mfma_i32_16x16x64_i8 v[110:113], v[130:133], v[206:209], v[110:113]
	v_mfma_i32_16x16x64_i8 v[106:109], v[164:167], v[206:209], v[106:109]
	v_mfma_i32_16x16x64_i8 v[94:97], v[130:133], v[214:217], v[94:97]
	v_mfma_i32_16x16x64_i8 v[90:93], v[164:167], v[214:217], v[90:93]
	v_mfma_i32_16x16x64_i8 v[78:81], v[130:133], v[222:225], v[78:81]
	v_mfma_i32_16x16x64_i8 v[74:77], v[164:167], v[222:225], v[74:77]
	v_mfma_i32_16x16x64_i8 v[126:129], v[134:137], v[202:205], v[126:129]
	v_mfma_i32_16x16x64_i8 v[122:125], v[168:171], v[202:205], v[122:125]
	v_mfma_i32_16x16x64_i8 v[110:113], v[134:137], v[210:213], v[110:113]
	v_mfma_i32_16x16x64_i8 v[106:109], v[168:171], v[210:213], v[106:109]
	v_mfma_i32_16x16x64_i8 v[94:97], v[134:137], v[218:221], v[94:97]
	v_mfma_i32_16x16x64_i8 v[90:93], v[168:171], v[218:221], v[90:93]
	v_mfma_i32_16x16x64_i8 v[78:81], v[134:137], v[226:229], v[78:81]
	v_mfma_i32_16x16x64_i8 v[74:77], v[168:171], v[226:229], v[74:77]
	v_mfma_i32_16x16x64_i8 v[118:121], v[172:175], v[192:195], v[118:121]
	v_mfma_i32_16x16x64_i8 v[114:117], v[184:187], v[192:195], v[114:117]
	v_mfma_i32_16x16x64_i8 v[102:105], v[172:175], v[206:209], v[102:105]
	v_mfma_i32_16x16x64_i8 v[98:101], v[184:187], v[206:209], v[98:101]
	v_mfma_i32_16x16x64_i8 v[86:89], v[172:175], v[214:217], v[86:89]
	v_mfma_i32_16x16x64_i8 v[82:85], v[184:187], v[214:217], v[82:85]
	v_mfma_i32_16x16x64_i8 v[70:73], v[172:175], v[222:225], v[70:73]
	v_mfma_i32_16x16x64_i8 v[66:69], v[184:187], v[222:225], v[66:69]
	v_mfma_i32_16x16x64_i8 v[118:121], v[176:179], v[202:205], v[118:121]
	v_mfma_i32_16x16x64_i8 v[114:117], v[188:191], v[202:205], v[114:117]
	v_mfma_i32_16x16x64_i8 v[102:105], v[176:179], v[210:213], v[102:105]
	v_mfma_i32_16x16x64_i8 v[98:101], v[188:191], v[210:213], v[98:101]
	v_mfma_i32_16x16x64_i8 v[86:89], v[176:179], v[218:221], v[86:89]
	v_mfma_i32_16x16x64_i8 v[82:85], v[188:191], v[218:221], v[82:85]
	v_mfma_i32_16x16x64_i8 v[70:73], v[176:179], v[226:229], v[70:73]
	v_mfma_i32_16x16x64_i8 v[66:69], v[188:191], v[226:229], v[66:69]
	s_barrier
	s_add_i32 s70, s54, s46
	v_lshl_add_u64 v[160:161], s[42:43], 0, v[140:141]
	s_mov_b32 m0, s70
	ds_read_b128 v[192:195], v183 offset:16384
	ds_read_b128 v[202:205], v183 offset:17408
	ds_read_b128 v[206:209], v183 offset:18432
	ds_read_b128 v[210:213], v183 offset:19456
	ds_read_b128 v[214:217], v183 offset:20480
	ds_read_b128 v[218:221], v183 offset:21504
	ds_read_b128 v[222:225], v183 offset:22528
	ds_read_b128 v[226:229], v183 offset:23552
	global_load_lds_dwordx4 v[160:161], off
	s_add_i32 m0, s70, 0x2000
	s_add_u32 s70, s42, 0x40000
	v_lshl_add_u64 v[198:199], s[42:43], 0, v[144:145]
	s_addc_u32 s71, s43, 0
	s_add_i32 s72, s55, s46
	global_load_lds_dwordx4 v[198:199], off
	v_lshl_add_u64 v[230:231], s[70:71], 0, v[140:141]
	s_mov_b32 m0, s72
	v_lshl_add_u64 v[232:233], s[44:45], 0, v[142:143]
	global_load_lds_dwordx4 v[230:231], off
	v_lshl_add_u64 v[230:231], s[70:71], 0, v[144:145]
	s_add_i32 m0, s72, 0x2000
	s_nop 0
	global_load_lds_dwordx4 v[230:231], off
	v_lshl_add_u64 v[230:231], s[44:45], 0, v[138:139]
	s_mov_b32 m0, s39
	s_nop 0
	global_load_lds_dwordx4 v[230:231], off
	s_mov_b32 m0, s47
	s_nop 0
	global_load_lds_dwordx4 v[232:233], off
	s_waitcnt vmcnt(8)
	s_waitcnt lgkmcnt(0)
	s_barrier
; #define PG8_STAGE(bufoff, gbase, voff) do { _Pragma("unroll") for (int _i = 0; _i < 2; ++_i) \
;         __builtin_amdgcn_global_load_lds((const unsigned*)((const char*)(gbase) + (voff)[_i]), (PG8_LAS unsigned*)(lds + (bufoff) + ldsw + _i * 8192), 16, 0, 0); } while (0)
; #define PG8_LDA(dst, b, h) do { _Pragma("unroll") for (int m = 0; m < 4; ++m) _Pragma("unroll") for (int k = 0; k < 2; ++k) dst[m][k] = *(const PG8_LAS bf16x8*)(lds + PG8_SA(b, h) + aoff + m * 2048 + k * 1024); } while (0)
; #define PG8_LDB(dst, b, h) do { _Pragma("unroll") for (int n = 0; n < 2; ++n) _Pragma("unroll") for (int k = 0; k < 2; ++k) dst[n][k] = *(const PG8_LAS bf16x8*)(lds + PG8_SB(b, h) + boff + n * 2048 + k * 1024); } while (0)
; #define PG8_MMA(ai, bj, At, Bt) do { __builtin_amdgcn_s_setprio(1); _Pragma("unroll") for (int m = 0; m < 4; ++m) _Pragma("unroll") for (int n = 0; n < 2; ++n) _Pragma("unroll") for (int k = 0; k < 2; ++k) \
;         acc[ai][bj][m][n] = mma16<I8>(Bt[n][k], At[m][k], acc[ai][bj][m][n]); __builtin_amdgcn_s_setprio(0); } while (0)
; #define PG8_WAIT_V(n) asm volatile("s_waitcnt vmcnt(" #n ")" ::: "memory")
; #define PG8_WAIT_L(n) asm volatile("s_waitcnt lgkmcnt(" #n ")" ::: "memory")
; #define PG8_BAR __builtin_amdgcn_s_barrier()
; #define PG8_SCHED __builtin_amdgcn_sched_barrier(0)
; template <class Epi, class Sched, bool ALIGN_EPI = false, bool SP2 = false, bool I8 = false>
; __device__ __forceinline__ void gemm_phase(PG8_LAS unsigned char* lds, const Gemm g, const Sched& S, const Epi& E) {
;     ...
;             PG8_WAIT_V(8); PG8_WAIT_L(0); PG8_BAR; PG8_MMA(1, 0, At, B0); PG8_MMA(1, 1, At, B1); PG8_BAR; PG8_SCHED;
;             PG8_LDB(B0, 1, 0); PG8_LDB(B1, 1, 1); PG8_SCHED; PG8_LDA(At, 1, 0); PG8_STAGE(PG8_SA(0, 1), a2 + hstep, voffA);
;             PG8_WAIT_V(8); PG8_WAIT_L(0); PG8_BAR; PG8_MMA(0, 0, At, B0); PG8_MMA(0, 1, At, B1); PG8_BAR; PG8_SCHED;
	s_waitcnt lgkmcnt(0)
	v_mfma_i32_16x16x64_i8 v[62:65], v[130:133], v[192:195], v[62:65]
	v_mfma_i32_16x16x64_i8 v[58:61], v[164:167], v[192:195], v[58:61]
	v_mfma_i32_16x16x64_i8 v[46:49], v[130:133], v[206:209], v[46:49]
	v_mfma_i32_16x16x64_i8 v[42:45], v[164:167], v[206:209], v[42:45]
	v_mfma_i32_16x16x64_i8 v[30:33], v[130:133], v[214:217], v[30:33]
	v_mfma_i32_16x16x64_i8 v[26:29], v[164:167], v[214:217], v[26:29]
	v_mfma_i32_16x16x64_i8 v[14:17], v[130:133], v[222:225], v[14:17]
	v_mfma_i32_16x16x64_i8 v[10:13], v[164:167], v[222:225], v[10:13]
	v_mfma_i32_16x16x64_i8 v[62:65], v[134:137], v[202:205], v[62:65]
	v_mfma_i32_16x16x64_i8 v[58:61], v[168:171], v[202:205], v[58:61]
	v_mfma_i32_16x16x64_i8 v[46:49], v[134:137], v[210:213], v[46:49]
	v_mfma_i32_16x16x64_i8 v[42:45], v[168:171], v[210:213], v[42:45]
	v_mfma_i32_16x16x64_i8 v[30:33], v[134:137], v[218:221], v[30:33]
	v_mfma_i32_16x16x64_i8 v[26:29], v[168:171], v[218:221], v[26:29]
	v_mfma_i32_16x16x64_i8 v[14:17], v[134:137], v[226:229], v[14:17]
	v_mfma_i32_16x16x64_i8 v[10:13], v[168:171], v[226:229], v[10:13]
	v_mfma_i32_16x16x64_i8 v[54:57], v[172:175], v[192:195], v[54:57]
	v_mfma_i32_16x16x64_i8 v[50:53], v[184:187], v[192:195], v[50:53]
	v_mfma_i32_16x16x64_i8 v[38:41], v[172:175], v[206:209], v[38:41]
	v_mfma_i32_16x16x64_i8 v[34:37], v[184:187], v[206:209], v[34:37]
	v_mfma_i32_16x16x64_i8 v[22:25], v[172:175], v[214:217], v[22:25]
	v_mfma_i32_16x16x64_i8 v[18:21], v[184:187], v[214:217], v[18:21]
	v_mfma_i32_16x16x64_i8 v[6:9], v[172:175], v[222:225], v[6:9]
	v_mfma_i32_16x16x64_i8 v[2:5], v[184:187], v[222:225], v[2:5]
	v_mfma_i32_16x16x64_i8 v[54:57], v[176:179], v[202:205], v[54:57]
	v_mfma_i32_16x16x64_i8 v[50:53], v[188:191], v[202:205], v[50:53]
	v_mfma_i32_16x16x64_i8 v[38:41], v[176:179], v[210:213], v[38:41]
	v_mfma_i32_16x16x64_i8 v[34:37], v[188:191], v[210:213], v[34:37]
	v_mfma_i32_16x16x64_i8 v[22:25], v[176:179], v[218:221], v[22:25]
	v_mfma_i32_16x16x64_i8 v[18:21], v[188:191], v[218:221], v[18:21]
	v_mfma_i32_16x16x64_i8 v[6:9], v[176:179], v[226:229], v[6:9]
	v_mfma_i32_16x16x64_i8 v[2:5], v[188:191], v[226:229], v[2:5]
	s_barrier
	s_add_i32 s70, 0, 0x18000
	v_add_u32_e32 v162, s70, v147
	s_add_i32 s71, 0, 0x1c000
	ds_read_b128 v[130:133], v162
	ds_read_b128 v[134:137], v162 offset:1024
	ds_read_b128 v[164:167], v162 offset:2048
	ds_read_b128 v[168:171], v162 offset:3072
	v_add_u32_e32 v162, s71, v147
	ds_read_b128 v[172:175], v162
	ds_read_b128 v[176:179], v162 offset:1024
	ds_read_b128 v[184:187], v162 offset:2048
	ds_read_b128 v[188:191], v162 offset:3072
	s_add_u32 s44, s44, 0x40000
	s_addc_u32 s45, s45, 0
	s_mov_b32 m0, s48
	v_lshl_add_u64 v[234:235], s[44:45], 0, v[138:139]
	ds_read_b128 v[192:195], v183 offset:32768
	ds_read_b128 v[202:205], v183 offset:33792
	ds_read_b128 v[206:209], v183 offset:34816
	ds_read_b128 v[210:213], v183 offset:35840
	ds_read_b128 v[214:217], v183 offset:36864
	ds_read_b128 v[218:221], v183 offset:37888
	ds_read_b128 v[222:225], v183 offset:38912
	ds_read_b128 v[226:229], v183 offset:39936
	global_load_lds_dwordx4 v[234:235], off
	v_lshl_add_u64 v[234:235], s[44:45], 0, v[142:143]
	s_mov_b32 m0, s49
	s_nop 0
	global_load_lds_dwordx4 v[234:235], off
	s_waitcnt vmcnt(8)
	s_waitcnt lgkmcnt(0)
	s_barrier
	s_waitcnt lgkmcnt(0)
	v_mfma_i32_16x16x64_i8 v[126:129], v[130:133], v[192:195], v[126:129]
	v_mfma_i32_16x16x64_i8 v[122:125], v[164:167], v[192:195], v[122:125]
	v_mfma_i32_16x16x64_i8 v[110:113], v[130:133], v[206:209], v[110:113]
	v_mfma_i32_16x16x64_i8 v[106:109], v[164:167], v[206:209], v[106:109]
	v_mfma_i32_16x16x64_i8 v[94:97], v[130:133], v[214:217], v[94:97]
	v_mfma_i32_16x16x64_i8 v[90:93], v[164:167], v[214:217], v[90:93]
	v_mfma_i32_16x16x64_i8 v[78:81], v[130:133], v[222:225], v[78:81]
	v_mfma_i32_16x16x64_i8 v[74:77], v[164:167], v[222:225], v[74:77]
	v_mfma_i32_16x16x64_i8 v[126:129], v[134:137], v[202:205], v[126:129]
	v_mfma_i32_16x16x64_i8 v[122:125], v[168:171], v[202:205], v[122:125]
	v_mfma_i32_16x16x64_i8 v[110:113], v[134:137], v[210:213], v[110:113]
	v_mfma_i32_16x16x64_i8 v[106:109], v[168:171], v[210:213], v[106:109]
	v_mfma_i32_16x16x64_i8 v[94:97], v[134:137], v[218:221], v[94:97]
	v_mfma_i32_16x16x64_i8 v[90:93], v[168:171], v[218:221], v[90:93]
	v_mfma_i32_16x16x64_i8 v[78:81], v[134:137], v[226:229], v[78:81]
	v_mfma_i32_16x16x64_i8 v[74:77], v[168:171], v[226:229], v[74:77]
	v_mfma_i32_16x16x64_i8 v[118:121], v[172:175], v[192:195], v[118:121]
	v_mfma_i32_16x16x64_i8 v[114:117], v[184:187], v[192:195], v[114:117]
	v_mfma_i32_16x16x64_i8 v[102:105], v[172:175], v[206:209], v[102:105]
	v_mfma_i32_16x16x64_i8 v[98:101], v[184:187], v[206:209], v[98:101]
	v_mfma_i32_16x16x64_i8 v[86:89], v[172:175], v[214:217], v[86:89]
	v_mfma_i32_16x16x64_i8 v[82:85], v[184:187], v[214:217], v[82:85]
	v_mfma_i32_16x16x64_i8 v[70:73], v[172:175], v[222:225], v[70:73]
	v_mfma_i32_16x16x64_i8 v[66:69], v[184:187], v[222:225], v[66:69]
	v_mfma_i32_16x16x64_i8 v[118:121], v[176:179], v[202:205], v[118:121]
	v_mfma_i32_16x16x64_i8 v[114:117], v[188:191], v[202:205], v[114:117]
	v_mfma_i32_16x16x64_i8 v[102:105], v[176:179], v[210:213], v[102:105]
	v_mfma_i32_16x16x64_i8 v[98:101], v[188:191], v[210:213], v[98:101]
	v_mfma_i32_16x16x64_i8 v[86:89], v[176:179], v[218:221], v[86:89]
	v_mfma_i32_16x16x64_i8 v[82:85], v[188:191], v[218:221], v[82:85]
	v_mfma_i32_16x16x64_i8 v[70:73], v[176:179], v[226:229], v[70:73]
	v_mfma_i32_16x16x64_i8 v[66:69], v[188:191], v[226:229], v[66:69]
	s_barrier
; #define PG8_STAGE(bufoff, gbase, voff) do { _Pragma("unroll") for (int _i = 0; _i < 2; ++_i) \
;         __builtin_amdgcn_global_load_lds((const unsigned*)((const char*)(gbase) + (voff)[_i]), (PG8_LAS unsigned*)(lds + (bufoff) + ldsw + _i * 8192), 16, 0, 0); } while (0)
; #define PG8_LDA(dst, b, h) do { _Pragma("unroll") for (int m = 0; m < 4; ++m) _Pragma("unroll") for (int k = 0; k < 2; ++k) dst[m][k] = *(const PG8_LAS bf16x8*)(lds + PG8_SA(b, h) + aoff + m * 2048 + k * 1024); } while (0)
; #define PG8_MMA(ai, bj, At, Bt) do { __builtin_amdgcn_s_setprio(1); _Pragma("unroll") for (int m = 0; m < 4; ++m) _Pragma("unroll") for (int n = 0; n < 2; ++n) _Pragma("unroll") for (int k = 0; k < 2; ++k) \
;         acc[ai][bj][m][n] = mma16<I8>(Bt[n][k], At[m][k], acc[ai][bj][m][n]); __builtin_amdgcn_s_setprio(0); } while (0)
; #define PG8_WAIT_V(n) asm volatile("s_waitcnt vmcnt(" #n ")" ::: "memory")
; #define PG8_WAIT_L(n) asm volatile("s_waitcnt lgkmcnt(" #n ")" ::: "memory")
; #define PG8_BAR __builtin_amdgcn_s_barrier()
; #define PG8_SCHED __builtin_amdgcn_sched_barrier(0)
; template <class Epi, class Sched, bool ALIGN_EPI = false, bool SP2 = false, bool I8 = false>
; __device__ __forceinline__ void gemm_phase(PG8_LAS unsigned char* lds, const Gemm g, const Sched& S, const Epi& E) {
;     ...
;         for (int t = 0; t < nt; t += 2) {
;             const bool last = (t == nt - 2);
;     ...
;             PG8_LDA(At, 1, 1); PG8_STAGE(PG8_SB(1, 0), b3, voffB); PG8_STAGE(PG8_SB(1, 1), b3 + hstep, voffB); PG8_STAGE(PG8_SA(1, 0), a3, voffA);
;             PG8_WAIT_V(8); PG8_WAIT_L(0); PG8_BAR; PG8_MMA(1, 0, At, B0); PG8_MMA(1, 1, At, B1); PG8_BAR; PG8_SCHED;
	s_add_i32 s44, s70, s46
	v_lshl_add_u64 v[160:161], v[160:161], 0, s[14:15]
	s_mov_b32 m0, s44
	ds_read_b128 v[192:195], v183 offset:49152
	ds_read_b128 v[202:205], v183 offset:50176
	ds_read_b128 v[206:209], v183 offset:51200
	ds_read_b128 v[210:213], v183 offset:52224
	ds_read_b128 v[214:217], v183 offset:53248
	ds_read_b128 v[218:221], v183 offset:54272
	ds_read_b128 v[222:225], v183 offset:55296
	ds_read_b128 v[226:229], v183 offset:56320
	global_load_lds_dwordx4 v[160:161], off
	s_add_i32 m0, s44, 0x2000
	s_add_u32 s42, s42, 0x40080
	v_lshl_add_u64 v[160:161], v[198:199], 0, s[14:15]
	s_addc_u32 s43, s43, 0
	s_add_i32 s44, s71, s46
	global_load_lds_dwordx4 v[160:161], off
	v_lshl_add_u64 v[160:161], s[42:43], 0, v[140:141]
	s_mov_b32 m0, s44
	s_nop 0
	global_load_lds_dwordx4 v[160:161], off
	v_lshl_add_u64 v[160:161], s[42:43], 0, v[144:145]
	s_add_i32 m0, s44, 0x2000
	s_nop 0
	global_load_lds_dwordx4 v[160:161], off
	v_lshl_add_u64 v[160:161], v[230:231], 0, s[14:15]
	s_mov_b32 m0, s51
	s_nop 0
	global_load_lds_dwordx4 v[160:161], off
	v_lshl_add_u64 v[160:161], v[232:233], 0, s[14:15]
	s_mov_b32 m0, s52
	s_nop 0
	global_load_lds_dwordx4 v[160:161], off
	s_waitcnt vmcnt(8)
	s_waitcnt lgkmcnt(0)
	s_barrier
	s_waitcnt lgkmcnt(0)
	v_mfma_i32_16x16x64_i8 v[62:65], v[130:133], v[192:195], v[62:65]
	v_mfma_i32_16x16x64_i8 v[58:61], v[164:167], v[192:195], v[58:61]
	v_mfma_i32_16x16x64_i8 v[46:49], v[130:133], v[206:209], v[46:49]
	v_mfma_i32_16x16x64_i8 v[42:45], v[164:167], v[206:209], v[42:45]
	v_mfma_i32_16x16x64_i8 v[30:33], v[130:133], v[214:217], v[30:33]
	v_mfma_i32_16x16x64_i8 v[26:29], v[164:167], v[214:217], v[26:29]
	v_mfma_i32_16x16x64_i8 v[14:17], v[130:133], v[222:225], v[14:17]
	v_mfma_i32_16x16x64_i8 v[10:13], v[164:167], v[222:225], v[10:13]
	v_mfma_i32_16x16x64_i8 v[62:65], v[134:137], v[202:205], v[62:65]
	v_mfma_i32_16x16x64_i8 v[58:61], v[168:171], v[202:205], v[58:61]
	v_mfma_i32_16x16x64_i8 v[46:49], v[134:137], v[210:213], v[46:49]
	v_mfma_i32_16x16x64_i8 v[42:45], v[168:171], v[210:213], v[42:45]
	v_mfma_i32_16x16x64_i8 v[30:33], v[134:137], v[218:221], v[30:33]
	v_mfma_i32_16x16x64_i8 v[26:29], v[168:171], v[218:221], v[26:29]
	v_mfma_i32_16x16x64_i8 v[14:17], v[134:137], v[226:229], v[14:17]
	v_mfma_i32_16x16x64_i8 v[10:13], v[168:171], v[226:229], v[10:13]
	v_mfma_i32_16x16x64_i8 v[54:57], v[172:175], v[192:195], v[54:57]
	v_mfma_i32_16x16x64_i8 v[50:53], v[184:187], v[192:195], v[50:53]
	v_mfma_i32_16x16x64_i8 v[38:41], v[172:175], v[206:209], v[38:41]
	v_mfma_i32_16x16x64_i8 v[34:37], v[184:187], v[206:209], v[34:37]
	v_mfma_i32_16x16x64_i8 v[22:25], v[172:175], v[214:217], v[22:25]
	v_mfma_i32_16x16x64_i8 v[18:21], v[184:187], v[214:217], v[18:21]
	v_mfma_i32_16x16x64_i8 v[6:9], v[172:175], v[222:225], v[6:9]
	v_mfma_i32_16x16x64_i8 v[2:5], v[184:187], v[222:225], v[2:5]
	v_mfma_i32_16x16x64_i8 v[54:57], v[176:179], v[202:205], v[54:57]
	v_mfma_i32_16x16x64_i8 v[50:53], v[188:191], v[202:205], v[50:53]
	v_mfma_i32_16x16x64_i8 v[38:41], v[176:179], v[210:213], v[38:41]
	v_mfma_i32_16x16x64_i8 v[34:37], v[188:191], v[210:213], v[34:37]
	v_mfma_i32_16x16x64_i8 v[22:25], v[176:179], v[218:221], v[22:25]
	v_mfma_i32_16x16x64_i8 v[18:21], v[188:191], v[218:221], v[18:21]
	v_mfma_i32_16x16x64_i8 v[6:9], v[176:179], v[226:229], v[6:9]
	v_mfma_i32_16x16x64_i8 v[2:5], v[188:191], v[226:229], v[2:5]
	s_barrier
	s_add_i32 s63, s63, 2
	s_add_u32 s40, s40, 0x100
	s_addc_u32 s41, s41, 0
	s_add_u32 s59, s59, 0x100
	s_addc_u32 s62, s62, 0
	s_cmp_gt_u32 s63, 13
	s_cbranch_scc0 .LBB0_974
	s_and_b64 vcc, exec, s[16:17]
	s_cbranch_vccz .LBB0_977
	s_barrier

; #define PG8_STAGE(bufoff, gbase, voff) do { _Pragma("unroll") for (int _i = 0; _i < 2; ++_i) \
;         __builtin_amdgcn_global_load_lds((const unsigned*)((const char*)(gbase) + (voff)[_i]), (PG8_LAS unsigned*)(lds + (bufoff) + ldsw + _i * 8192), 16, 0, 0); } while (0)
; #define PG8_LDA(dst, b, h) do { _Pragma("unroll") for (int m = 0; m < 4; ++m) _Pragma("unroll") for (int k = 0; k < 2; ++k) dst[m][k] = *(const PG8_LAS bf16x8*)(lds + PG8_SA(b, h) + aoff + m * 2048 + k * 1024); } while (0)
; #define PG8_LDB(dst, b, h) do { _Pragma("unroll") for (int n = 0; n < 2; ++n) _Pragma("unroll") for (int k = 0; k < 2; ++k) dst[n][k] = *(const PG8_LAS bf16x8*)(lds + PG8_SB(b, h) + boff + n * 2048 + k * 1024); } while (0)
; #define PG8_MMA(ai, bj, At, Bt) do { __builtin_amdgcn_s_setprio(1); _Pragma("unroll") for (int m = 0; m < 4; ++m) _Pragma("unroll") for (int n = 0; n < 2; ++n) _Pragma("unroll") for (int k = 0; k < 2; ++k) \
;         acc[ai][bj][m][n] = mma16<I8>(Bt[n][k], At[m][k], acc[ai][bj][m][n]); __builtin_amdgcn_s_setprio(0); } while (0)
; #define PG8_WAIT_V(n) asm volatile("s_waitcnt vmcnt(" #n ")" ::: "memory")
; #define PG8_WAIT_L(n) asm volatile("s_waitcnt lgkmcnt(" #n ")" ::: "memory")
; #define PG8_BAR __builtin_amdgcn_s_barrier()
; #define PG8_SCHED __builtin_amdgcn_sched_barrier(0)
; template <class Epi, class Sched, bool ALIGN_EPI = false, bool SP2 = false, bool I8 = false>
; __device__ __forceinline__ void gemm_phase(PG8_LAS unsigned char* lds, const Gemm g, const Sched& S, const Epi& E) {
;     ...
;             PG8_LDB(B0, 0, 0); PG8_LDB(B1, 0, 1); PG8_SCHED; PG8_LDA(At, 0, 0); PG8_STAGE(PG8_SA(1, 1), a1 + hstep, voffA);
;             PG8_WAIT_V(8); PG8_WAIT_L(0); PG8_BAR; PG8_MMA(0, 0, At, B0); PG8_MMA(0, 1, At, B1); PG8_BAR; PG8_SCHED;
;             PG8_LDA(At, 0, 1); PG8_STAGE(PG8_SB(0, 0), b2, voffB); PG8_STAGE(PG8_SB(0, 1), b2 + hstep, voffB); PG8_STAGE(PG8_SA(0, 0), a2, voffA);
;             PG8_WAIT_V(8); PG8_WAIT_L(0); PG8_BAR; PG8_MMA(1, 0, At, B0); PG8_MMA(1, 1, At, B1); PG8_BAR; PG8_SCHED;
.LBB0_1112:
	ds_read_b128 v[34:37], v196
	ds_read_b128 v[38:41], v196 offset:1024
	ds_read_b128 v[50:53], v196 offset:2048
	ds_read_b128 v[54:57], v196 offset:3072
	ds_read_b128 v[168:171], v198
	ds_read_b128 v[172:175], v198 offset:1024
	ds_read_b128 v[176:179], v198 offset:2048
	ds_read_b128 v[180:183], v198 offset:3072
	s_add_u32 s48, s46, 0xfffc0080
	s_addc_u32 s49, s47, -1
	s_cmp_eq_u32 s62, 12
	s_cselect_b32 s51, s5, s49
	s_cselect_b32 s50, s33, s48
	s_cselect_b32 s49, s39, s59
	s_cselect_b32 s48, s41, s58
	v_lshl_add_u64 v[222:223], s[46:47], 0, v[160:161]
	s_add_i32 m0, s3, 0xc000
	ds_read_b128 v[184:187], v199
	ds_read_b128 v[188:191], v199 offset:1024
	ds_read_b128 v[192:195], v199 offset:2048
	ds_read_b128 v[202:205], v199 offset:3072
	ds_read_b128 v[206:209], v199 offset:4096
	ds_read_b128 v[210:213], v199 offset:5120
	ds_read_b128 v[214:217], v199 offset:6144
	ds_read_b128 v[218:221], v199 offset:7168
	global_load_lds_dwordx4 v[222:223], off
	v_lshl_add_u64 v[222:223], s[46:47], 0, v[162:163]
	s_add_i32 m0, s3, 0xe000
	s_nop 0
	global_load_lds_dwordx4 v[222:223], off
	s_waitcnt vmcnt(8)
	s_waitcnt lgkmcnt(0)
	s_barrier
	s_waitcnt lgkmcnt(0)
	v_mfma_i32_16x16x64_i8 v[142:145], v[34:37], v[184:187], v[142:145]
	v_mfma_i32_16x16x64_i8 v[138:141], v[50:53], v[184:187], v[138:141]
	v_mfma_i32_16x16x64_i8 v[126:129], v[34:37], v[192:195], v[126:129]
	v_mfma_i32_16x16x64_i8 v[122:125], v[50:53], v[192:195], v[122:125]
	v_mfma_i32_16x16x64_i8 v[110:113], v[34:37], v[206:209], v[110:113]
	v_mfma_i32_16x16x64_i8 v[106:109], v[50:53], v[206:209], v[106:109]
	v_mfma_i32_16x16x64_i8 v[94:97], v[34:37], v[214:217], v[94:97]
	v_mfma_i32_16x16x64_i8 v[90:93], v[50:53], v[214:217], v[90:93]
	v_mfma_i32_16x16x64_i8 v[142:145], v[38:41], v[188:191], v[142:145]
	v_mfma_i32_16x16x64_i8 v[138:141], v[54:57], v[188:191], v[138:141]
	v_mfma_i32_16x16x64_i8 v[126:129], v[38:41], v[202:205], v[126:129]
	v_mfma_i32_16x16x64_i8 v[122:125], v[54:57], v[202:205], v[122:125]
	v_mfma_i32_16x16x64_i8 v[110:113], v[38:41], v[210:213], v[110:113]
	v_mfma_i32_16x16x64_i8 v[106:109], v[54:57], v[210:213], v[106:109]
	v_mfma_i32_16x16x64_i8 v[94:97], v[38:41], v[218:221], v[94:97]
	v_mfma_i32_16x16x64_i8 v[90:93], v[54:57], v[218:221], v[90:93]
	v_mfma_i32_16x16x64_i8 v[134:137], v[168:171], v[184:187], v[134:137]
	v_mfma_i32_16x16x64_i8 v[130:133], v[176:179], v[184:187], v[130:133]
	v_mfma_i32_16x16x64_i8 v[118:121], v[168:171], v[192:195], v[118:121]
	v_mfma_i32_16x16x64_i8 v[114:117], v[176:179], v[192:195], v[114:117]
	v_mfma_i32_16x16x64_i8 v[102:105], v[168:171], v[206:209], v[102:105]
	v_mfma_i32_16x16x64_i8 v[98:101], v[176:179], v[206:209], v[98:101]
	v_mfma_i32_16x16x64_i8 v[86:89], v[168:171], v[214:217], v[86:89]
	v_mfma_i32_16x16x64_i8 v[82:85], v[176:179], v[214:217], v[82:85]
	v_mfma_i32_16x16x64_i8 v[134:137], v[172:175], v[188:191], v[134:137]
	v_mfma_i32_16x16x64_i8 v[130:133], v[180:183], v[188:191], v[130:133]
	v_mfma_i32_16x16x64_i8 v[118:121], v[172:175], v[202:205], v[118:121]
	v_mfma_i32_16x16x64_i8 v[114:117], v[180:183], v[202:205], v[114:117]
	v_mfma_i32_16x16x64_i8 v[102:105], v[172:175], v[210:213], v[102:105]
	v_mfma_i32_16x16x64_i8 v[98:101], v[180:183], v[210:213], v[98:101]
	v_mfma_i32_16x16x64_i8 v[86:89], v[172:175], v[218:221], v[86:89]
	v_mfma_i32_16x16x64_i8 v[82:85], v[180:183], v[218:221], v[82:85]
	s_barrier
	s_add_i32 s63, s54, s15
	v_lshl_add_u64 v[222:223], s[48:49], 0, v[154:155]
	s_mov_b32 m0, s63
	ds_read_b128 v[184:187], v199 offset:16384
	ds_read_b128 v[188:191], v199 offset:17408
	ds_read_b128 v[192:195], v199 offset:18432
	ds_read_b128 v[202:205], v199 offset:19456
	ds_read_b128 v[206:209], v199 offset:20480
	ds_read_b128 v[210:213], v199 offset:21504
	ds_read_b128 v[214:217], v199 offset:22528
	ds_read_b128 v[218:221], v199 offset:23552
	global_load_lds_dwordx4 v[222:223], off
	s_add_i32 m0, s63, 0x2000
	s_add_u32 s70, s48, 0x40000
	v_lshl_add_u64 v[224:225], s[48:49], 0, v[158:159]
	s_addc_u32 s71, s49, 0
	s_add_i32 s63, s55, s15
	global_load_lds_dwordx4 v[224:225], off
	v_lshl_add_u64 v[226:227], s[70:71], 0, v[154:155]
	s_mov_b32 m0, s63
	v_lshl_add_u64 v[228:229], s[50:51], 0, v[156:157]
	global_load_lds_dwordx4 v[226:227], off
	v_lshl_add_u64 v[226:227], s[70:71], 0, v[158:159]
	s_add_i32 m0, s63, 0x2000
	s_nop 0
	global_load_lds_dwordx4 v[226:227], off
	v_lshl_add_u64 v[226:227], s[50:51], 0, v[152:153]
	s_mov_b32 m0, s3
	s_nop 0
	global_load_lds_dwordx4 v[226:227], off
	s_mov_b32 m0, s17
	s_nop 0
	global_load_lds_dwordx4 v[228:229], off
	s_waitcnt vmcnt(8)
	s_waitcnt lgkmcnt(0)
	s_barrier
; #define PG8_STAGE(bufoff, gbase, voff) do { _Pragma("unroll") for (int _i = 0; _i < 2; ++_i) \
;         __builtin_amdgcn_global_load_lds((const unsigned*)((const char*)(gbase) + (voff)[_i]), (PG8_LAS unsigned*)(lds + (bufoff) + ldsw + _i * 8192), 16, 0, 0); } while (0)
; #define PG8_LDA(dst, b, h) do { _Pragma("unroll") for (int m = 0; m < 4; ++m) _Pragma("unroll") for (int k = 0; k < 2; ++k) dst[m][k] = *(const PG8_LAS bf16x8*)(lds + PG8_SA(b, h) + aoff + m * 2048 + k * 1024); } while (0)
; #define PG8_LDB(dst, b, h) do { _Pragma("unroll") for (int n = 0; n < 2; ++n) _Pragma("unroll") for (int k = 0; k < 2; ++k) dst[n][k] = *(const PG8_LAS bf16x8*)(lds + PG8_SB(b, h) + boff + n * 2048 + k * 1024); } while (0)
; #define PG8_MMA(ai, bj, At, Bt) do { __builtin_amdgcn_s_setprio(1); _Pragma("unroll") for (int m = 0; m < 4; ++m) _Pragma("unroll") for (int n = 0; n < 2; ++n) _Pragma("unroll") for (int k = 0; k < 2; ++k) \
;         acc[ai][bj][m][n] = mma16<I8>(Bt[n][k], At[m][k], acc[ai][bj][m][n]); __builtin_amdgcn_s_setprio(0); } while (0)
; #define PG8_WAIT_V(n) asm volatile("s_waitcnt vmcnt(" #n ")" ::: "memory")
; #define PG8_WAIT_L(n) asm volatile("s_waitcnt lgkmcnt(" #n ")" ::: "memory")
; #define PG8_BAR __builtin_amdgcn_s_barrier()
; #define PG8_SCHED __builtin_amdgcn_sched_barrier(0)
; template <class Epi, class Sched, bool ALIGN_EPI = false, bool SP2 = false, bool I8 = false>
; __device__ __forceinline__ void gemm_phase(PG8_LAS unsigned char* lds, const Gemm g, const Sched& S, const Epi& E) {
;     ...
;             PG8_WAIT_V(8); PG8_WAIT_L(0); PG8_BAR; PG8_MMA(1, 0, At, B0); PG8_MMA(1, 1, At, B1); PG8_BAR; PG8_SCHED;
;             PG8_LDB(B0, 1, 0); PG8_LDB(B1, 1, 1); PG8_SCHED; PG8_LDA(At, 1, 0); PG8_STAGE(PG8_SA(0, 1), a2 + hstep, voffA);
;             PG8_WAIT_V(8); PG8_WAIT_L(0); PG8_BAR; PG8_MMA(0, 0, At, B0); PG8_MMA(0, 1, At, B1); PG8_BAR; PG8_SCHED;
	s_waitcnt lgkmcnt(0)
	v_mfma_i32_16x16x64_i8 v[78:81], v[34:37], v[184:187], v[78:81]
	v_mfma_i32_16x16x64_i8 v[74:77], v[50:53], v[184:187], v[74:77]
	v_mfma_i32_16x16x64_i8 v[62:65], v[34:37], v[192:195], v[62:65]
	v_mfma_i32_16x16x64_i8 v[58:61], v[50:53], v[192:195], v[58:61]
	v_mfma_i32_16x16x64_i8 v[30:33], v[34:37], v[206:209], v[30:33]
	v_mfma_i32_16x16x64_i8 v[26:29], v[50:53], v[206:209], v[26:29]
	v_mfma_i32_16x16x64_i8 v[14:17], v[34:37], v[214:217], v[14:17]
	v_mfma_i32_16x16x64_i8 v[10:13], v[50:53], v[214:217], v[10:13]
	v_mfma_i32_16x16x64_i8 v[78:81], v[38:41], v[188:191], v[78:81]
	v_mfma_i32_16x16x64_i8 v[74:77], v[54:57], v[188:191], v[74:77]
	v_mfma_i32_16x16x64_i8 v[62:65], v[38:41], v[202:205], v[62:65]
	v_mfma_i32_16x16x64_i8 v[58:61], v[54:57], v[202:205], v[58:61]
	v_mfma_i32_16x16x64_i8 v[30:33], v[38:41], v[210:213], v[30:33]
	v_mfma_i32_16x16x64_i8 v[26:29], v[54:57], v[210:213], v[26:29]
	v_mfma_i32_16x16x64_i8 v[14:17], v[38:41], v[218:221], v[14:17]
	v_mfma_i32_16x16x64_i8 v[10:13], v[54:57], v[218:221], v[10:13]
	v_mfma_i32_16x16x64_i8 v[46:49], v[168:171], v[192:195], v[46:49]
	v_mfma_i32_16x16x64_i8 v[42:45], v[176:179], v[192:195], v[42:45]
	v_mfma_i32_16x16x64_i8 v[22:25], v[168:171], v[206:209], v[22:25]
	v_mfma_i32_16x16x64_i8 v[18:21], v[176:179], v[206:209], v[18:21]
	v_mfma_i32_16x16x64_i8 v[6:9], v[168:171], v[214:217], v[6:9]
	v_mfma_i32_16x16x64_i8 v[2:5], v[176:179], v[214:217], v[2:5]
	v_mfma_i32_16x16x64_i8 v[34:37], v[168:171], v[184:187], v[70:73]
	v_mfma_i32_16x16x64_i8 v[38:41], v[176:179], v[184:187], v[66:69]
	v_mfma_i32_16x16x64_i8 v[46:49], v[172:175], v[202:205], v[46:49]
	v_mfma_i32_16x16x64_i8 v[42:45], v[180:183], v[202:205], v[42:45]
	v_mfma_i32_16x16x64_i8 v[22:25], v[172:175], v[210:213], v[22:25]
	v_mfma_i32_16x16x64_i8 v[18:21], v[180:183], v[210:213], v[18:21]
	v_mfma_i32_16x16x64_i8 v[6:9], v[172:175], v[218:221], v[6:9]
	v_mfma_i32_16x16x64_i8 v[2:5], v[180:183], v[218:221], v[2:5]
	v_mfma_i32_16x16x64_i8 v[34:37], v[172:175], v[188:191], v[34:37]
	v_mfma_i32_16x16x64_i8 v[38:41], v[180:183], v[188:191], v[38:41]
	s_barrier
	s_add_i32 s63, 0, 0x18000
	s_add_i32 s70, 0, 0x1c000
	v_add_u32_e32 v70, s63, v147
	v_add_u32_e32 v180, s70, v147
	ds_read_b128 v[50:53], v70
	ds_read_b128 v[54:57], v70 offset:1024
	ds_read_b128 v[66:69], v70 offset:2048
	ds_read_b128 v[70:73], v70 offset:3072
	ds_read_b128 v[168:171], v180
	ds_read_b128 v[172:175], v180 offset:1024
	ds_read_b128 v[176:179], v180 offset:2048
	ds_read_b128 v[180:183], v180 offset:3072
	s_add_u32 s50, s50, 0x40000
	s_addc_u32 s51, s51, 0
	s_mov_b32 m0, s25
	v_lshl_add_u64 v[230:231], s[50:51], 0, v[152:153]
	ds_read_b128 v[184:187], v199 offset:32768
	ds_read_b128 v[188:191], v199 offset:33792
	ds_read_b128 v[192:195], v199 offset:34816
	ds_read_b128 v[202:205], v199 offset:35840
	ds_read_b128 v[206:209], v199 offset:36864
	ds_read_b128 v[210:213], v199 offset:37888
	ds_read_b128 v[214:217], v199 offset:38912
	ds_read_b128 v[218:221], v199 offset:39936
	global_load_lds_dwordx4 v[230:231], off
	v_lshl_add_u64 v[230:231], s[50:51], 0, v[156:157]
	s_mov_b32 m0, s27
	s_nop 0
	global_load_lds_dwordx4 v[230:231], off
	s_waitcnt vmcnt(8)
	s_waitcnt lgkmcnt(0)
	s_barrier
	s_waitcnt lgkmcnt(0)
	v_mfma_i32_16x16x64_i8 v[142:145], v[50:53], v[184:187], v[142:145]
	v_mfma_i32_16x16x64_i8 v[138:141], v[66:69], v[184:187], v[138:141]
	v_mfma_i32_16x16x64_i8 v[126:129], v[50:53], v[192:195], v[126:129]
	v_mfma_i32_16x16x64_i8 v[122:125], v[66:69], v[192:195], v[122:125]
	v_mfma_i32_16x16x64_i8 v[110:113], v[50:53], v[206:209], v[110:113]
	v_mfma_i32_16x16x64_i8 v[106:109], v[66:69], v[206:209], v[106:109]
	v_mfma_i32_16x16x64_i8 v[94:97], v[50:53], v[214:217], v[94:97]
	v_mfma_i32_16x16x64_i8 v[90:93], v[66:69], v[214:217], v[90:93]
	v_mfma_i32_16x16x64_i8 v[142:145], v[54:57], v[188:191], v[142:145]
	v_mfma_i32_16x16x64_i8 v[138:141], v[70:73], v[188:191], v[138:141]
	v_mfma_i32_16x16x64_i8 v[126:129], v[54:57], v[202:205], v[126:129]
	v_mfma_i32_16x16x64_i8 v[122:125], v[70:73], v[202:205], v[122:125]
	v_mfma_i32_16x16x64_i8 v[110:113], v[54:57], v[210:213], v[110:113]
	v_mfma_i32_16x16x64_i8 v[106:109], v[70:73], v[210:213], v[106:109]
	v_mfma_i32_16x16x64_i8 v[94:97], v[54:57], v[218:221], v[94:97]
	v_mfma_i32_16x16x64_i8 v[90:93], v[70:73], v[218:221], v[90:93]
	v_mfma_i32_16x16x64_i8 v[134:137], v[168:171], v[184:187], v[134:137]
	v_mfma_i32_16x16x64_i8 v[130:133], v[176:179], v[184:187], v[130:133]
	v_mfma_i32_16x16x64_i8 v[118:121], v[168:171], v[192:195], v[118:121]
	v_mfma_i32_16x16x64_i8 v[114:117], v[176:179], v[192:195], v[114:117]
	v_mfma_i32_16x16x64_i8 v[102:105], v[168:171], v[206:209], v[102:105]
	v_mfma_i32_16x16x64_i8 v[98:101], v[176:179], v[206:209], v[98:101]
	v_mfma_i32_16x16x64_i8 v[86:89], v[168:171], v[214:217], v[86:89]
	v_mfma_i32_16x16x64_i8 v[82:85], v[176:179], v[214:217], v[82:85]
	v_mfma_i32_16x16x64_i8 v[134:137], v[172:175], v[188:191], v[134:137]
	v_mfma_i32_16x16x64_i8 v[130:133], v[180:183], v[188:191], v[130:133]
	v_mfma_i32_16x16x64_i8 v[118:121], v[172:175], v[202:205], v[118:121]
	v_mfma_i32_16x16x64_i8 v[114:117], v[180:183], v[202:205], v[114:117]
	v_mfma_i32_16x16x64_i8 v[102:105], v[172:175], v[210:213], v[102:105]
	v_mfma_i32_16x16x64_i8 v[98:101], v[180:183], v[210:213], v[98:101]
	v_mfma_i32_16x16x64_i8 v[86:89], v[172:175], v[218:221], v[86:89]
	v_mfma_i32_16x16x64_i8 v[82:85], v[180:183], v[218:221], v[82:85]
	s_barrier
; #define PG8_STAGE(bufoff, gbase, voff) do { _Pragma("unroll") for (int _i = 0; _i < 2; ++_i) \
;         __builtin_amdgcn_global_load_lds((const unsigned*)((const char*)(gbase) + (voff)[_i]), (PG8_LAS unsigned*)(lds + (bufoff) + ldsw + _i * 8192), 16, 0, 0); } while (0)
; #define PG8_LDA(dst, b, h) do { _Pragma("unroll") for (int m = 0; m < 4; ++m) _Pragma("unroll") for (int k = 0; k < 2; ++k) dst[m][k] = *(const PG8_LAS bf16x8*)(lds + PG8_SA(b, h) + aoff + m * 2048 + k * 1024); } while (0)
; #define PG8_MMA(ai, bj, At, Bt) do { __builtin_amdgcn_s_setprio(1); _Pragma("unroll") for (int m = 0; m < 4; ++m) _Pragma("unroll") for (int n = 0; n < 2; ++n) _Pragma("unroll") for (int k = 0; k < 2; ++k) \
;         acc[ai][bj][m][n] = mma16<I8>(Bt[n][k], At[m][k], acc[ai][bj][m][n]); __builtin_amdgcn_s_setprio(0); } while (0)
; #define PG8_WAIT_V(n) asm volatile("s_waitcnt vmcnt(" #n ")" ::: "memory")
; #define PG8_WAIT_L(n) asm volatile("s_waitcnt lgkmcnt(" #n ")" ::: "memory")
; #define PG8_BAR __builtin_amdgcn_s_barrier()
; #define PG8_SCHED __builtin_amdgcn_sched_barrier(0)
; template <class Epi, class Sched, bool ALIGN_EPI = false, bool SP2 = false, bool I8 = false>
; __device__ __forceinline__ void gemm_phase(PG8_LAS unsigned char* lds, const Gemm g, const Sched& S, const Epi& E) {
;     ...
;         for (int t = 0; t < nt; t += 2) {
;     ...
;             PG8_LDA(At, 1, 1); PG8_STAGE(PG8_SB(1, 0), b3, voffB); PG8_STAGE(PG8_SB(1, 1), b3 + hstep, voffB); PG8_STAGE(PG8_SA(1, 0), a3, voffA);
;             PG8_WAIT_V(8); PG8_WAIT_L(0); PG8_BAR; PG8_MMA(1, 0, At, B0); PG8_MMA(1, 1, At, B1); PG8_BAR; PG8_SCHED;
	s_add_i32 s50, s63, s15
	v_lshl_add_u64 v[222:223], v[222:223], 0, s[10:11]
	s_mov_b32 m0, s50
	ds_read_b128 v[184:187], v199 offset:49152
	ds_read_b128 v[188:191], v199 offset:50176
	ds_read_b128 v[192:195], v199 offset:51200
	ds_read_b128 v[202:205], v199 offset:52224
	ds_read_b128 v[206:209], v199 offset:53248
	ds_read_b128 v[210:213], v199 offset:54272
	ds_read_b128 v[214:217], v199 offset:55296
	ds_read_b128 v[218:221], v199 offset:56320
	global_load_lds_dwordx4 v[222:223], off
	s_add_i32 m0, s50, 0x2000
	s_add_u32 s48, s48, 0x40080
	v_lshl_add_u64 v[222:223], v[224:225], 0, s[10:11]
	s_addc_u32 s49, s49, 0
	s_add_i32 s50, s70, s15
	global_load_lds_dwordx4 v[222:223], off
	v_lshl_add_u64 v[222:223], s[48:49], 0, v[154:155]
	s_mov_b32 m0, s50
	s_nop 0
	global_load_lds_dwordx4 v[222:223], off
	v_lshl_add_u64 v[222:223], s[48:49], 0, v[158:159]
	s_add_i32 m0, s50, 0x2000
	s_nop 0
	global_load_lds_dwordx4 v[222:223], off
	v_lshl_add_u64 v[222:223], v[226:227], 0, s[10:11]
	s_mov_b32 m0, s31
	s_nop 0
	global_load_lds_dwordx4 v[222:223], off
	v_lshl_add_u64 v[222:223], v[228:229], 0, s[10:11]
	s_mov_b32 m0, s35
	s_nop 0
	global_load_lds_dwordx4 v[222:223], off
	s_waitcnt vmcnt(8)
	s_waitcnt lgkmcnt(0)
	s_barrier
	s_waitcnt lgkmcnt(0)
	v_mfma_i32_16x16x64_i8 v[78:81], v[50:53], v[184:187], v[78:81]
	v_mfma_i32_16x16x64_i8 v[74:77], v[66:69], v[184:187], v[74:77]
	v_mfma_i32_16x16x64_i8 v[62:65], v[50:53], v[192:195], v[62:65]
	v_mfma_i32_16x16x64_i8 v[58:61], v[66:69], v[192:195], v[58:61]
	v_mfma_i32_16x16x64_i8 v[30:33], v[50:53], v[206:209], v[30:33]
	v_mfma_i32_16x16x64_i8 v[26:29], v[66:69], v[206:209], v[26:29]
	v_mfma_i32_16x16x64_i8 v[14:17], v[50:53], v[214:217], v[14:17]
	v_mfma_i32_16x16x64_i8 v[10:13], v[66:69], v[214:217], v[10:13]
	v_mfma_i32_16x16x64_i8 v[78:81], v[54:57], v[188:191], v[78:81]
	v_mfma_i32_16x16x64_i8 v[74:77], v[70:73], v[188:191], v[74:77]
	v_mfma_i32_16x16x64_i8 v[62:65], v[54:57], v[202:205], v[62:65]
	v_mfma_i32_16x16x64_i8 v[58:61], v[70:73], v[202:205], v[58:61]
	v_mfma_i32_16x16x64_i8 v[30:33], v[54:57], v[210:213], v[30:33]
	v_mfma_i32_16x16x64_i8 v[26:29], v[70:73], v[210:213], v[26:29]
	v_mfma_i32_16x16x64_i8 v[14:17], v[54:57], v[218:221], v[14:17]
	v_mfma_i32_16x16x64_i8 v[10:13], v[70:73], v[218:221], v[10:13]
	v_mfma_i32_16x16x64_i8 v[34:37], v[168:171], v[184:187], v[34:37]
	v_mfma_i32_16x16x64_i8 v[70:73], v[172:175], v[188:191], v[34:37]
	v_mfma_i32_16x16x64_i8 v[34:37], v[176:179], v[184:187], v[38:41]
	v_mfma_i32_16x16x64_i8 v[66:69], v[180:183], v[188:191], v[34:37]
	v_mfma_i32_16x16x64_i8 v[34:37], v[168:171], v[192:195], v[46:49]
	v_mfma_i32_16x16x64_i8 v[46:49], v[172:175], v[202:205], v[34:37]
	v_mfma_i32_16x16x64_i8 v[34:37], v[176:179], v[192:195], v[42:45]
	v_mfma_i32_16x16x64_i8 v[22:25], v[168:171], v[206:209], v[22:25]
	v_mfma_i32_16x16x64_i8 v[18:21], v[176:179], v[206:209], v[18:21]
	v_mfma_i32_16x16x64_i8 v[6:9], v[168:171], v[214:217], v[6:9]
	v_mfma_i32_16x16x64_i8 v[2:5], v[176:179], v[214:217], v[2:5]
	v_mfma_i32_16x16x64_i8 v[42:45], v[180:183], v[202:205], v[34:37]
	v_mfma_i32_16x16x64_i8 v[22:25], v[172:175], v[210:213], v[22:25]
	v_mfma_i32_16x16x64_i8 v[18:21], v[180:183], v[210:213], v[18:21]
	v_mfma_i32_16x16x64_i8 v[6:9], v[172:175], v[218:221], v[6:9]
	v_mfma_i32_16x16x64_i8 v[2:5], v[180:183], v[218:221], v[2:5]
	s_barrier
	s_add_i32 s62, s62, 2
	s_add_u32 s46, s46, 0x100
	s_addc_u32 s47, s47, 0
	s_add_u32 s58, s58, 0x100
	s_addc_u32 s59, s59, 0
	s_cmp_gt_u32 s62, 13
	s_cbranch_scc0 .LBB0_1112
	s_and_b64 vcc, exec, s[12:13]
	s_cbranch_vccz .LBB0_1115
	s_barrier
